# baseline (speedup 1.0000x reference)
.LBB5_140:
	v_lshl_or_b32 v2, s42, 3, v187
	v_ashrrev_i32_e32 v3, 31, v2
	v_lshlrev_b64 v[2:3], 16, v[2:3]
	v_lshl_add_u64 v[2:3], s[48:49], 0, v[2:3]
	v_mov_b32_e32 v169, 0
	v_lshlrev_b32_e32 v168, 4, v189
	s_or_b32 s25, s2, s50
	s_or_b32 s24, s50, 1
	s_mov_b32 s1, 0
	v_lshl_add_u64 v[166:167], v[2:3], 0, v[168:169]
	s_lshl_b32 s0, s25, 12
	s_or_b32 s30, s2, s24
	v_lshl_add_u64 v[18:19], v[166:167], 0, s[0:1]
	s_lshl_b32 s0, s30, 12
	v_lshl_add_u64 v[34:35], v[166:167], 0, s[0:1]
	s_waitcnt vmcnt(8)
	v_mov_b32_e32 v2, v200
	v_mov_b32_e32 v3, v201
	v_mov_b32_e32 v4, v202
	v_mov_b32_e32 v5, v203
	v_mov_b32_e32 v6, v204
	v_mov_b32_e32 v7, v205
	v_mov_b32_e32 v8, v206
	v_mov_b32_e32 v9, v207
	v_mov_b32_e32 v10, v208
	v_mov_b32_e32 v11, v209
	v_mov_b32_e32 v12, v210
	v_mov_b32_e32 v13, v211
	v_mov_b32_e32 v14, v212
	v_mov_b32_e32 v15, v213
	v_mov_b32_e32 v16, v214
	v_mov_b32_e32 v17, v215
	v_mov_b32_e32 v18, v216
	v_mov_b32_e32 v19, v217
	v_mov_b32_e32 v20, v218
	v_mov_b32_e32 v21, v219
	v_mov_b32_e32 v22, v220
	v_mov_b32_e32 v23, v221
	v_mov_b32_e32 v24, v222
	v_mov_b32_e32 v25, v223
	v_mov_b32_e32 v26, v224
	v_mov_b32_e32 v27, v225
	v_mov_b32_e32 v28, v226
	v_mov_b32_e32 v29, v227
	v_mov_b32_e32 v30, v228
	v_mov_b32_e32 v31, v229
	v_mov_b32_e32 v32, v230
	v_mov_b32_e32 v33, v231
	v_or_b32_e32 v52, v147, v146
	s_add_i32 s0, s59, 2
	s_and_b32 s28, s0, 6
	s_or_b32 s31, s2, s28
	s_lshl_b32 s0, s31, 12
	v_lshl_add_u64 v[50:51], v[166:167], 0, s[0:1]
	s_waitcnt lgkmcnt(0)
	s_barrier
	global_load_dwordx4 v[34:37], v[50:51], off
	global_load_dwordx4 v[38:41], v[50:51], off offset:1024
	global_load_dwordx4 v[42:45], v[50:51], off offset:2048
	global_load_dwordx4 v[46:49], v[50:51], off offset:3072
	v_xad_u32 v191, v52, v152, 0
	v_lshl_add_u32 v122, s25, 10, v191
	ds_read_b128 v[50:53], v122
	ds_read_b128 v[54:57], v122 offset:16384
	ds_read_b128 v[58:61], v122 offset:32768
	ds_read_b128 v[62:65], v122 offset:49152
	s_waitcnt vmcnt(19) lgkmcnt(3)
	v_mfma_f32_16x16x32_f16 v[66:69], v[2:5], v[50:53], 0
	s_waitcnt vmcnt(18)
	v_mfma_f32_16x16x32_f16 v[70:73], v[6:9], v[50:53], 0
	s_waitcnt vmcnt(17)
	v_mfma_f32_16x16x32_f16 v[74:77], v[10:13], v[50:53], 0
	s_waitcnt vmcnt(16)
	v_mfma_f32_16x16x32_f16 v[50:53], v[14:17], v[50:53], 0
	s_waitcnt lgkmcnt(2)
	v_mfma_f32_16x16x32_f16 v[78:81], v[2:5], v[54:57], 0
	v_mfma_f32_16x16x32_f16 v[82:85], v[6:9], v[54:57], 0
	v_mfma_f32_16x16x32_f16 v[86:89], v[10:13], v[54:57], 0
	v_mfma_f32_16x16x32_f16 v[54:57], v[14:17], v[54:57], 0
	s_waitcnt lgkmcnt(1)
	v_mfma_f32_16x16x32_f16 v[90:93], v[2:5], v[58:61], 0
	v_mfma_f32_16x16x32_f16 v[94:97], v[6:9], v[58:61], 0
	v_mfma_f32_16x16x32_f16 v[98:101], v[10:13], v[58:61], 0
	v_mfma_f32_16x16x32_f16 v[58:61], v[14:17], v[58:61], 0
	s_waitcnt lgkmcnt(0)
	v_mfma_f32_16x16x32_f16 v[102:105], v[2:5], v[62:65], 0
	v_mfma_f32_16x16x32_f16 v[106:109], v[6:9], v[62:65], 0
	v_mfma_f32_16x16x32_f16 v[110:113], v[10:13], v[62:65], 0
	v_mfma_f32_16x16x32_f16 v[62:65], v[14:17], v[62:65], 0
	v_add_u32_e32 v114, 0x10000, v122
	v_add_u32_e32 v118, 0x14000, v122
	v_add_u32_e32 v123, 0x18000, v122
	v_add_u32_e32 v126, 0x1c000, v122
	ds_read_b128 v[114:117], v114
	ds_read_b128 v[118:121], v118
	ds_read_b128 v[122:125], v123
	ds_read_b128 v[126:129], v126
	s_waitcnt lgkmcnt(3)
	v_mfma_f32_16x16x32_f16 v[130:133], v[2:5], v[114:117], 0
	v_mfma_f32_16x16x32_f16 v[134:137], v[6:9], v[114:117], 0
	v_mfma_f32_16x16x32_f16 v[138:141], v[10:13], v[114:117], 0
	v_mfma_f32_16x16x32_f16 v[114:117], v[14:17], v[114:117], 0
	s_waitcnt lgkmcnt(2)
	v_mfma_f32_16x16x32_f16 v[142:145], v[2:5], v[118:121], 0
	v_mfma_f32_16x16x32_f16 v[146:149], v[6:9], v[118:121], 0
	v_mfma_f32_16x16x32_f16 v[150:153], v[10:13], v[118:121], 0
	v_mfma_f32_16x16x32_f16 v[118:121], v[14:17], v[118:121], 0
	s_waitcnt lgkmcnt(1)
	v_mfma_f32_16x16x32_f16 v[154:157], v[2:5], v[122:125], 0
	v_mfma_f32_16x16x32_f16 v[158:161], v[6:9], v[122:125], 0
	v_mfma_f32_16x16x32_f16 v[170:173], v[10:13], v[122:125], 0
	v_mfma_f32_16x16x32_f16 v[122:125], v[14:17], v[122:125], 0
	s_waitcnt lgkmcnt(0)
	v_mfma_f32_16x16x32_f16 v[2:5], v[2:5], v[126:129], 0
	v_mfma_f32_16x16x32_f16 v[6:9], v[6:9], v[126:129], 0
	v_mfma_f32_16x16x32_f16 v[10:13], v[10:13], v[126:129], 0
	v_mfma_f32_16x16x32_f16 v[14:17], v[14:17], v[126:129], 0
	s_add_i32 s0, s50, 3
	s_and_b32 s29, s0, 7
	s_or_b32 s48, s29, s2
	s_lshl_b32 s0, s48, 12
	v_lshl_add_u64 v[178:179], v[166:167], 0, s[0:1]
	global_load_dwordx4 v[126:129], v[178:179], off
	global_load_dwordx4 v[174:177], v[178:179], off offset:1024
	global_load_dwordx4 v[192:195], v[178:179], off offset:2048
	global_load_dwordx4 v[196:199], v[178:179], off offset:3072
	v_lshl_add_u32 v163, s30, 10, v191
	ds_read_b128 v[200:203], v163
	ds_read_b128 v[204:207], v163 offset:16384
	ds_read_b128 v[208:211], v163 offset:32768
	ds_read_b128 v[212:215], v163 offset:49152
	s_waitcnt vmcnt(19) lgkmcnt(3)
	v_mfma_f32_16x16x32_f16 v[66:69], v[18:21], v[200:203], v[66:69]
	s_waitcnt vmcnt(18)
	v_mfma_f32_16x16x32_f16 v[70:73], v[22:25], v[200:203], v[70:73]
	s_waitcnt vmcnt(17)
	v_mfma_f32_16x16x32_f16 v[74:77], v[26:29], v[200:203], v[74:77]
	s_waitcnt vmcnt(16)
	v_mfma_f32_16x16x32_f16 v[50:53], v[30:33], v[200:203], v[50:53]
	s_waitcnt lgkmcnt(2)
	v_mfma_f32_16x16x32_f16 v[78:81], v[18:21], v[204:207], v[78:81]
	v_mfma_f32_16x16x32_f16 v[82:85], v[22:25], v[204:207], v[82:85]
	v_mfma_f32_16x16x32_f16 v[86:89], v[26:29], v[204:207], v[86:89]
	v_mfma_f32_16x16x32_f16 v[54:57], v[30:33], v[204:207], v[54:57]
	s_waitcnt lgkmcnt(1)
	v_mfma_f32_16x16x32_f16 v[90:93], v[18:21], v[208:211], v[90:93]
	v_mfma_f32_16x16x32_f16 v[94:97], v[22:25], v[208:211], v[94:97]
	v_mfma_f32_16x16x32_f16 v[98:101], v[26:29], v[208:211], v[98:101]
	v_mfma_f32_16x16x32_f16 v[58:61], v[30:33], v[208:211], v[58:61]
	s_waitcnt lgkmcnt(0)
	v_mfma_f32_16x16x32_f16 v[102:105], v[18:21], v[212:215], v[102:105]
	v_mfma_f32_16x16x32_f16 v[106:109], v[22:25], v[212:215], v[106:109]
	v_mfma_f32_16x16x32_f16 v[110:113], v[26:29], v[212:215], v[110:113]
	v_mfma_f32_16x16x32_f16 v[62:65], v[30:33], v[212:215], v[62:65]
	v_add_u32_e32 v165, 0x10000, v163
	v_add_u32_e32 v168, 0x14000, v163
	ds_read_b128 v[200:203], v165
	ds_read_b128 v[204:207], v168
	v_add_u32_e32 v165, 0x18000, v163
	v_add_u32_e32 v163, 0x1c000, v163
	ds_read_b128 v[208:211], v165
	ds_read_b128 v[212:215], v163
	s_waitcnt lgkmcnt(3)
	v_mfma_f32_16x16x32_f16 v[130:133], v[18:21], v[200:203], v[130:133]
	v_mfma_f32_16x16x32_f16 v[134:137], v[22:25], v[200:203], v[134:137]
	v_mfma_f32_16x16x32_f16 v[138:141], v[26:29], v[200:203], v[138:141]
	v_mfma_f32_16x16x32_f16 v[114:117], v[30:33], v[200:203], v[114:117]
	s_waitcnt lgkmcnt(2)
	v_mfma_f32_16x16x32_f16 v[142:145], v[18:21], v[204:207], v[142:145]
	v_mfma_f32_16x16x32_f16 v[146:149], v[22:25], v[204:207], v[146:149]
	v_mfma_f32_16x16x32_f16 v[150:153], v[26:29], v[204:207], v[150:153]
	v_mfma_f32_16x16x32_f16 v[118:121], v[30:33], v[204:207], v[118:121]
	s_waitcnt lgkmcnt(1)
	v_mfma_f32_16x16x32_f16 v[154:157], v[18:21], v[208:211], v[154:157]
	v_mfma_f32_16x16x32_f16 v[158:161], v[22:25], v[208:211], v[158:161]
	v_mfma_f32_16x16x32_f16 v[122:125], v[30:33], v[208:211], v[122:125]
	s_waitcnt lgkmcnt(0)
	v_mfma_f32_16x16x32_f16 v[2:5], v[18:21], v[212:215], v[2:5]
	v_mfma_f32_16x16x32_f16 v[6:9], v[22:25], v[212:215], v[6:9]
	v_mfma_f32_16x16x32_f16 v[10:13], v[26:29], v[212:215], v[10:13]
	v_mfma_f32_16x16x32_f16 v[14:17], v[30:33], v[212:215], v[14:17]
	v_mfma_f32_16x16x32_f16 v[170:173], v[26:29], v[208:211], v[170:173]
	s_xor_b32 s25, s25, 4
	s_lshl_b32 s0, s25, 12
	v_lshl_add_u64 v[30:31], v[166:167], 0, s[0:1]
	s_waitcnt vmcnt(8)
	s_barrier
	s_getreg_b32 s80, hwreg(HW_REG_XCC_ID, 0, 4)
	s_and_b32 s80, s80, 15
	s_add_i32 s80, s80, 1
	s_lshl_b32 s81, s34, 3
	s_or_b32 s81, s81, s33
	s_lshl_b32 s81, s81, 7
	s_add_u32 s82, s46, s81
	s_addc_u32 s83, s47, 0
	v_mov_b32_e32 v254, 0
	v_mov_b32_e32 v255, s80
	s_and_saveexec_b64 s[84:85], s[4:5]
	global_store_dword v254, v255, s[82:83] sc1
	s_mov_b64 exec, s[84:85]
	global_load_dwordx4 v[18:21], v[30:31], off
	global_load_dwordx4 v[22:25], v[30:31], off offset:1024
	global_load_dwordx4 v[26:29], v[30:31], off offset:2048
	s_nop 0
	global_load_dwordx4 v[30:33], v[30:31], off offset:3072
	v_lshl_add_u32 v163, s31, 10, v191
	ds_read_b128 v[200:203], v163
	ds_read_b128 v[204:207], v163 offset:16384
	ds_read_b128 v[208:211], v163 offset:32768
	ds_read_b128 v[212:215], v163 offset:49152
	s_waitcnt vmcnt(11) lgkmcnt(3)
	v_mfma_f32_16x16x32_f16 v[66:69], v[34:37], v[200:203], v[66:69]
	s_waitcnt vmcnt(10)
	v_mfma_f32_16x16x32_f16 v[70:73], v[38:41], v[200:203], v[70:73]
	s_waitcnt vmcnt(9)
	v_mfma_f32_16x16x32_f16 v[74:77], v[42:45], v[200:203], v[74:77]
	s_waitcnt vmcnt(8)
	v_mfma_f32_16x16x32_f16 v[50:53], v[46:49], v[200:203], v[50:53]
	s_waitcnt lgkmcnt(2)
	v_mfma_f32_16x16x32_f16 v[78:81], v[34:37], v[204:207], v[78:81]
	v_mfma_f32_16x16x32_f16 v[82:85], v[38:41], v[204:207], v[82:85]
	v_mfma_f32_16x16x32_f16 v[86:89], v[42:45], v[204:207], v[86:89]
	v_mfma_f32_16x16x32_f16 v[54:57], v[46:49], v[204:207], v[54:57]
	s_waitcnt lgkmcnt(1)
	v_mfma_f32_16x16x32_f16 v[90:93], v[34:37], v[208:211], v[90:93]
	v_mfma_f32_16x16x32_f16 v[94:97], v[38:41], v[208:211], v[94:97]
	v_mfma_f32_16x16x32_f16 v[98:101], v[42:45], v[208:211], v[98:101]
	v_mfma_f32_16x16x32_f16 v[58:61], v[46:49], v[208:211], v[58:61]
	s_waitcnt lgkmcnt(0)
	v_mfma_f32_16x16x32_f16 v[102:105], v[34:37], v[212:215], v[102:105]
	v_mfma_f32_16x16x32_f16 v[106:109], v[38:41], v[212:215], v[106:109]
	v_mfma_f32_16x16x32_f16 v[110:113], v[42:45], v[212:215], v[110:113]
	v_mfma_f32_16x16x32_f16 v[62:65], v[46:49], v[212:215], v[62:65]
	v_add_u32_e32 v165, 0x10000, v163
	v_add_u32_e32 v168, 0x14000, v163
	ds_read_b128 v[200:203], v165
	ds_read_b128 v[204:207], v168
	v_add_u32_e32 v165, 0x18000, v163
	v_add_u32_e32 v163, 0x1c000, v163
	ds_read_b128 v[208:211], v165
	ds_read_b128 v[212:215], v163
	s_waitcnt lgkmcnt(3)
	v_mfma_f32_16x16x32_f16 v[130:133], v[34:37], v[200:203], v[130:133]
	v_mfma_f32_16x16x32_f16 v[134:137], v[38:41], v[200:203], v[134:137]
	v_mfma_f32_16x16x32_f16 v[138:141], v[42:45], v[200:203], v[138:141]
	v_mfma_f32_16x16x32_f16 v[114:117], v[46:49], v[200:203], v[114:117]
	s_waitcnt lgkmcnt(2)
	v_mfma_f32_16x16x32_f16 v[142:145], v[34:37], v[204:207], v[142:145]
	v_mfma_f32_16x16x32_f16 v[146:149], v[38:41], v[204:207], v[146:149]
	v_mfma_f32_16x16x32_f16 v[150:153], v[42:45], v[204:207], v[150:153]
	v_mfma_f32_16x16x32_f16 v[118:121], v[46:49], v[204:207], v[118:121]
	s_waitcnt lgkmcnt(1)
	v_mfma_f32_16x16x32_f16 v[154:157], v[34:37], v[208:211], v[154:157]
	v_mfma_f32_16x16x32_f16 v[158:161], v[38:41], v[208:211], v[158:161]
	v_mfma_f32_16x16x32_f16 v[122:125], v[46:49], v[208:211], v[122:125]
	s_waitcnt lgkmcnt(0)
	v_mfma_f32_16x16x32_f16 v[2:5], v[34:37], v[212:215], v[2:5]
	v_mfma_f32_16x16x32_f16 v[6:9], v[38:41], v[212:215], v[6:9]
	v_mfma_f32_16x16x32_f16 v[10:13], v[42:45], v[212:215], v[10:13]
	v_mfma_f32_16x16x32_f16 v[14:17], v[46:49], v[212:215], v[14:17]
	v_mfma_f32_16x16x32_f16 v[170:173], v[42:45], v[208:211], v[170:173]
	s_add_i32 s0, s50, 5
	s_and_b32 s30, s0, 7
	s_or_b32 s49, s30, s2
	s_lshl_b32 s0, s49, 12
	v_lshl_add_u64 v[46:47], v[166:167], 0, s[0:1]
	global_load_dwordx4 v[34:37], v[46:47], off
	global_load_dwordx4 v[38:41], v[46:47], off offset:1024
	global_load_dwordx4 v[42:45], v[46:47], off offset:2048
	s_nop 0
	global_load_dwordx4 v[46:49], v[46:47], off offset:3072
	v_lshl_add_u32 v163, s48, 10, v191
	ds_read_b128 v[200:203], v163
	ds_read_b128 v[204:207], v163 offset:16384
	ds_read_b128 v[208:211], v163 offset:32768
	ds_read_b128 v[212:215], v163 offset:49152
	s_waitcnt vmcnt(11) lgkmcnt(3)
	v_mfma_f32_16x16x32_f16 v[66:69], v[126:129], v[200:203], v[66:69]
	s_waitcnt vmcnt(10)
	v_mfma_f32_16x16x32_f16 v[70:73], v[174:177], v[200:203], v[70:73]
	s_waitcnt vmcnt(9)
	v_mfma_f32_16x16x32_f16 v[74:77], v[192:195], v[200:203], v[74:77]
	s_waitcnt vmcnt(8)
	v_mfma_f32_16x16x32_f16 v[50:53], v[196:199], v[200:203], v[50:53]
	s_waitcnt lgkmcnt(2)
	v_mfma_f32_16x16x32_f16 v[78:81], v[126:129], v[204:207], v[78:81]
	v_mfma_f32_16x16x32_f16 v[82:85], v[174:177], v[204:207], v[82:85]
	v_mfma_f32_16x16x32_f16 v[86:89], v[192:195], v[204:207], v[86:89]
	v_mfma_f32_16x16x32_f16 v[54:57], v[196:199], v[204:207], v[54:57]
	s_waitcnt lgkmcnt(1)
	v_mfma_f32_16x16x32_f16 v[90:93], v[126:129], v[208:211], v[90:93]
	v_mfma_f32_16x16x32_f16 v[94:97], v[174:177], v[208:211], v[94:97]
	v_mfma_f32_16x16x32_f16 v[98:101], v[192:195], v[208:211], v[98:101]
	v_mfma_f32_16x16x32_f16 v[58:61], v[196:199], v[208:211], v[58:61]
	s_waitcnt lgkmcnt(0)
	v_mfma_f32_16x16x32_f16 v[102:105], v[126:129], v[212:215], v[102:105]
	v_mfma_f32_16x16x32_f16 v[106:109], v[174:177], v[212:215], v[106:109]
	v_mfma_f32_16x16x32_f16 v[110:113], v[192:195], v[212:215], v[110:113]
	v_mfma_f32_16x16x32_f16 v[62:65], v[196:199], v[212:215], v[62:65]
	v_add_u32_e32 v165, 0x10000, v163
	v_add_u32_e32 v168, 0x14000, v163
	ds_read_b128 v[200:203], v165
	ds_read_b128 v[204:207], v168
	v_add_u32_e32 v165, 0x18000, v163
	v_add_u32_e32 v163, 0x1c000, v163
	ds_read_b128 v[208:211], v165
	ds_read_b128 v[212:215], v163
	s_waitcnt lgkmcnt(3)
	v_mfma_f32_16x16x32_f16 v[130:133], v[126:129], v[200:203], v[130:133]
	v_mfma_f32_16x16x32_f16 v[134:137], v[174:177], v[200:203], v[134:137]
	v_mfma_f32_16x16x32_f16 v[138:141], v[192:195], v[200:203], v[138:141]
	v_mfma_f32_16x16x32_f16 v[114:117], v[196:199], v[200:203], v[114:117]
	s_waitcnt lgkmcnt(2)
	v_mfma_f32_16x16x32_f16 v[142:145], v[126:129], v[204:207], v[142:145]
	v_mfma_f32_16x16x32_f16 v[146:149], v[174:177], v[204:207], v[146:149]
	v_mfma_f32_16x16x32_f16 v[150:153], v[192:195], v[204:207], v[150:153]
	v_mfma_f32_16x16x32_f16 v[118:121], v[196:199], v[204:207], v[118:121]
	s_waitcnt lgkmcnt(1)
	v_mfma_f32_16x16x32_f16 v[154:157], v[126:129], v[208:211], v[154:157]
	v_mfma_f32_16x16x32_f16 v[158:161], v[174:177], v[208:211], v[158:161]
	v_mfma_f32_16x16x32_f16 v[122:125], v[196:199], v[208:211], v[122:125]
	s_waitcnt lgkmcnt(0)
	v_mfma_f32_16x16x32_f16 v[2:5], v[126:129], v[212:215], v[2:5]
	v_mfma_f32_16x16x32_f16 v[6:9], v[174:177], v[212:215], v[6:9]
	v_mfma_f32_16x16x32_f16 v[10:13], v[192:195], v[212:215], v[10:13]
	v_mfma_f32_16x16x32_f16 v[14:17], v[196:199], v[212:215], v[14:17]
	v_mfma_f32_16x16x32_f16 v[170:173], v[192:195], v[208:211], v[170:173]
	s_add_i32 s59, s59, 6
	s_and_b32 s31, s59, 6
	s_or_b32 s52, s2, s31
	s_lshl_b32 s0, s52, 12
	v_lshl_add_u64 v[178:179], v[166:167], 0, s[0:1]
	s_lshl_b32 s86, s34, 3
	s_or_b32 s86, s86, s33
	s_xor_b32 s86, s86, 1
	s_lshl_b32 s86, s86, 7
	s_add_u32 s86, s46, s86
	s_addc_u32 s87, s47, 0
	v_mov_b32_e32 v254, 0
	global_load_dword v254, v254, s[86:87] sc1
	global_load_dwordx4 v[126:129], v[178:179], off
	global_load_dwordx4 v[174:177], v[178:179], off offset:1024
	global_load_dwordx4 v[192:195], v[178:179], off offset:2048
	global_load_dwordx4 v[196:199], v[178:179], off offset:3072
	v_lshl_add_u32 v163, s25, 10, v191
	ds_read_b128 v[200:203], v163
	ds_read_b128 v[204:207], v163 offset:16384
	ds_read_b128 v[208:211], v163 offset:32768
	ds_read_b128 v[212:215], v163 offset:49152
	s_waitcnt vmcnt(12) lgkmcnt(3)
	v_mfma_f32_16x16x32_f16 v[66:69], v[18:21], v[200:203], v[66:69]
	s_waitcnt vmcnt(11)
	v_mfma_f32_16x16x32_f16 v[70:73], v[22:25], v[200:203], v[70:73]
	s_waitcnt vmcnt(10)
	v_mfma_f32_16x16x32_f16 v[74:77], v[26:29], v[200:203], v[74:77]
	s_waitcnt vmcnt(9)
	v_mfma_f32_16x16x32_f16 v[50:53], v[30:33], v[200:203], v[50:53]
	s_waitcnt lgkmcnt(2)
	v_mfma_f32_16x16x32_f16 v[78:81], v[18:21], v[204:207], v[78:81]
	v_mfma_f32_16x16x32_f16 v[82:85], v[22:25], v[204:207], v[82:85]
	v_mfma_f32_16x16x32_f16 v[86:89], v[26:29], v[204:207], v[86:89]
	v_mfma_f32_16x16x32_f16 v[54:57], v[30:33], v[204:207], v[54:57]
	s_waitcnt lgkmcnt(1)
	v_mfma_f32_16x16x32_f16 v[90:93], v[18:21], v[208:211], v[90:93]
	v_mfma_f32_16x16x32_f16 v[94:97], v[22:25], v[208:211], v[94:97]
	v_mfma_f32_16x16x32_f16 v[98:101], v[26:29], v[208:211], v[98:101]
	v_mfma_f32_16x16x32_f16 v[58:61], v[30:33], v[208:211], v[58:61]
	s_waitcnt lgkmcnt(0)
	v_mfma_f32_16x16x32_f16 v[102:105], v[18:21], v[212:215], v[102:105]
	v_mfma_f32_16x16x32_f16 v[106:109], v[22:25], v[212:215], v[106:109]
	v_mfma_f32_16x16x32_f16 v[110:113], v[26:29], v[212:215], v[110:113]
	v_mfma_f32_16x16x32_f16 v[62:65], v[30:33], v[212:215], v[62:65]
	v_add_u32_e32 v165, 0x10000, v163
	v_add_u32_e32 v168, 0x14000, v163
	ds_read_b128 v[200:203], v165
	ds_read_b128 v[204:207], v168
	v_add_u32_e32 v165, 0x18000, v163
	v_add_u32_e32 v163, 0x1c000, v163
	ds_read_b128 v[208:211], v165
	ds_read_b128 v[212:215], v163
	s_waitcnt lgkmcnt(3)
	v_mfma_f32_16x16x32_f16 v[130:133], v[18:21], v[200:203], v[130:133]
	v_mfma_f32_16x16x32_f16 v[134:137], v[22:25], v[200:203], v[134:137]
	v_mfma_f32_16x16x32_f16 v[138:141], v[26:29], v[200:203], v[138:141]
	v_mfma_f32_16x16x32_f16 v[114:117], v[30:33], v[200:203], v[114:117]
	s_waitcnt lgkmcnt(2)
	v_mfma_f32_16x16x32_f16 v[142:145], v[18:21], v[204:207], v[142:145]
	v_mfma_f32_16x16x32_f16 v[146:149], v[22:25], v[204:207], v[146:149]
	v_mfma_f32_16x16x32_f16 v[150:153], v[26:29], v[204:207], v[150:153]
	v_mfma_f32_16x16x32_f16 v[118:121], v[30:33], v[204:207], v[118:121]
	s_waitcnt lgkmcnt(1)
	v_mfma_f32_16x16x32_f16 v[154:157], v[18:21], v[208:211], v[154:157]
	v_mfma_f32_16x16x32_f16 v[158:161], v[22:25], v[208:211], v[158:161]
	v_mfma_f32_16x16x32_f16 v[122:125], v[30:33], v[208:211], v[122:125]
	s_waitcnt lgkmcnt(0)
	v_mfma_f32_16x16x32_f16 v[2:5], v[18:21], v[212:215], v[2:5]
	v_mfma_f32_16x16x32_f16 v[6:9], v[22:25], v[212:215], v[6:9]
	v_mfma_f32_16x16x32_f16 v[10:13], v[26:29], v[212:215], v[10:13]
	v_mfma_f32_16x16x32_f16 v[14:17], v[30:33], v[212:215], v[14:17]
	v_mfma_f32_16x16x32_f16 v[170:173], v[26:29], v[208:211], v[170:173]
	s_add_i32 s0, s50, -1
	s_and_b32 s48, s0, 7
	s_or_b32 s25, s48, s2
	s_lshl_b32 s0, s25, 12
	v_lshl_add_u64 v[18:19], v[166:167], 0, s[0:1]
	global_load_dwordx4 v[200:203], v[18:19], off
	global_load_dwordx4 v[204:207], v[18:19], off offset:1024
	global_load_dwordx4 v[208:211], v[18:19], off offset:2048
	global_load_dwordx4 v[212:215], v[18:19], off offset:3072
	v_lshl_add_u32 v163, s49, 10, v191
	ds_read_b128 v[18:21], v163
	ds_read_b128 v[22:25], v163 offset:16384
	ds_read_b128 v[26:29], v163 offset:32768
	ds_read_b128 v[30:33], v163 offset:49152
	s_waitcnt vmcnt(12) lgkmcnt(3)
	v_mfma_f32_16x16x32_f16 v[66:69], v[34:37], v[18:21], v[66:69]
	s_waitcnt vmcnt(11)
	v_mfma_f32_16x16x32_f16 v[70:73], v[38:41], v[18:21], v[70:73]
	s_waitcnt vmcnt(10)
	v_mfma_f32_16x16x32_f16 v[74:77], v[42:45], v[18:21], v[74:77]
	s_waitcnt vmcnt(9)
	v_mfma_f32_16x16x32_f16 v[18:21], v[46:49], v[18:21], v[50:53]
	s_waitcnt lgkmcnt(2)
	v_mfma_f32_16x16x32_f16 v[50:53], v[34:37], v[22:25], v[78:81]
	v_mfma_f32_16x16x32_f16 v[78:81], v[38:41], v[22:25], v[82:85]
	v_mfma_f32_16x16x32_f16 v[82:85], v[42:45], v[22:25], v[86:89]
	v_mfma_f32_16x16x32_f16 v[22:25], v[46:49], v[22:25], v[54:57]
	s_waitcnt lgkmcnt(1)
	v_mfma_f32_16x16x32_f16 v[54:57], v[34:37], v[26:29], v[90:93]
	v_mfma_f32_16x16x32_f16 v[86:89], v[38:41], v[26:29], v[94:97]
	v_mfma_f32_16x16x32_f16 v[90:93], v[42:45], v[26:29], v[98:101]
	v_mfma_f32_16x16x32_f16 v[26:29], v[46:49], v[26:29], v[58:61]
	s_waitcnt lgkmcnt(0)
	v_mfma_f32_16x16x32_f16 v[58:61], v[34:37], v[30:33], v[102:105]
	v_mfma_f32_16x16x32_f16 v[94:97], v[38:41], v[30:33], v[106:109]
	v_mfma_f32_16x16x32_f16 v[98:101], v[42:45], v[30:33], v[110:113]
	v_mfma_f32_16x16x32_f16 v[30:33], v[46:49], v[30:33], v[62:65]
	s_nop 1
	v_add_u32_e32 v62, 0x10000, v163
	v_add_u32_e32 v102, 0x14000, v163
	v_add_u32_e32 v106, 0x18000, v163
	v_add_u32_e32 v110, 0x1c000, v163
	ds_read_b128 v[62:65], v62
	ds_read_b128 v[102:105], v102
	ds_read_b128 v[106:109], v106
	ds_read_b128 v[110:113], v110
	s_waitcnt lgkmcnt(3)
	v_mfma_f32_16x16x32_f16 v[130:133], v[34:37], v[62:65], v[130:133]
	v_mfma_f32_16x16x32_f16 v[134:137], v[38:41], v[62:65], v[134:137]
	v_mfma_f32_16x16x32_f16 v[138:141], v[42:45], v[62:65], v[138:141]
	v_mfma_f32_16x16x32_f16 v[62:65], v[46:49], v[62:65], v[114:117]
	s_waitcnt lgkmcnt(2)
	v_mfma_f32_16x16x32_f16 v[114:117], v[34:37], v[102:105], v[142:145]
	v_mfma_f32_16x16x32_f16 v[142:145], v[38:41], v[102:105], v[146:149]
	v_mfma_f32_16x16x32_f16 v[146:149], v[42:45], v[102:105], v[150:153]
	v_mfma_f32_16x16x32_f16 v[102:105], v[46:49], v[102:105], v[118:121]
	s_waitcnt lgkmcnt(1)
	v_mfma_f32_16x16x32_f16 v[118:121], v[34:37], v[106:109], v[154:157]
	v_mfma_f32_16x16x32_f16 v[150:153], v[38:41], v[106:109], v[158:161]
	v_mfma_f32_16x16x32_f16 v[154:157], v[42:45], v[106:109], v[170:173]
	v_mfma_f32_16x16x32_f16 v[106:109], v[46:49], v[106:109], v[122:125]
	s_waitcnt lgkmcnt(0)
	v_mfma_f32_16x16x32_f16 v[34:37], v[34:37], v[110:113], v[2:5]
	v_mfma_f32_16x16x32_f16 v[38:41], v[38:41], v[110:113], v[6:9]
	v_mfma_f32_16x16x32_f16 v[42:45], v[42:45], v[110:113], v[10:13]
	v_mfma_f32_16x16x32_f16 v[46:49], v[46:49], v[110:113], v[14:17]
	s_xor_b32 s2, s58, 1
	s_lshl_b32 s49, s2, 3
	s_or_b32 s51, s49, s50
	s_lshl_b32 s0, s51, 12
	v_lshl_add_u64 v[14:15], v[166:167], 0, s[0:1]
	s_waitcnt vmcnt(8)
	s_barrier
	v_lshlrev_b32_e32 v255, 4, v0
	v_readfirstlane_b32 s92, v0
	s_lshl_b32 s92, s92, 4
	s_xor_b32 s93, s58, 1
	s_lshl_b32 s94, s93, 13
	s_add_i32 s92, s92, s94
	s_lshl_b32 s94, s34, 3
	s_or_b32 s94, s94, s33
	s_xor_b32 s94, s94, 1
	s_lshl_b32 s94, s94, 16
	s_add_u32 s88, s26, s94
	s_addc_u32 s89, s27, 0
	s_add_i32 s95, s92, 0x0
	s_mov_b32 m0, s95
	s_add_u32 s84, s88, 0x0
	s_addc_u32 s85, s89, 0
	global_load_lds_dwordx4 v255, s[84:85] sc0 sc1
	s_add_i32 s95, s92, 0x4000
	s_mov_b32 m0, s95
	s_add_u32 s84, s88, 0x2000
	s_addc_u32 s85, s89, 0
	global_load_lds_dwordx4 v255, s[84:85] sc0 sc1
	s_add_i32 s95, s92, 0x8000
	s_mov_b32 m0, s95
	s_add_u32 s84, s88, 0x4000
	s_addc_u32 s85, s89, 0
	global_load_lds_dwordx4 v255, s[84:85] sc0 sc1
	s_add_i32 s95, s92, 0xc000
	s_mov_b32 m0, s95
	s_add_u32 s84, s88, 0x6000
	s_addc_u32 s85, s89, 0
	global_load_lds_dwordx4 v255, s[84:85] sc0 sc1
	s_add_i32 s95, s92, 0x10000
	s_mov_b32 m0, s95
	s_add_u32 s84, s88, 0x8000
	s_addc_u32 s85, s89, 0
	global_load_lds_dwordx4 v255, s[84:85] sc0 sc1
	s_add_i32 s95, s92, 0x14000
	s_mov_b32 m0, s95
	s_add_u32 s84, s88, 0xa000
	s_addc_u32 s85, s89, 0
	global_load_lds_dwordx4 v255, s[84:85] sc0 sc1
	s_add_i32 s95, s92, 0x18000
	s_mov_b32 m0, s95
	s_add_u32 s84, s88, 0xc000
	s_addc_u32 s85, s89, 0
	global_load_lds_dwordx4 v255, s[84:85] sc0 sc1
	s_add_i32 s95, s92, 0x1c000
	s_mov_b32 m0, s95
	s_add_u32 s84, s88, 0xe000
	s_addc_u32 s85, s89, 0
	global_load_lds_dwordx4 v255, s[84:85] sc0 sc1
	global_load_dwordx4 v[2:5], v[14:15], off
	global_load_dwordx4 v[6:9], v[14:15], off offset:1024
	global_load_dwordx4 v[10:13], v[14:15], off offset:2048
	s_nop 0
	global_load_dwordx4 v[14:17], v[14:15], off offset:3072
	v_lshl_add_u32 v163, s52, 10, v191
	ds_read_b128 v[110:113], v163
	ds_read_b128 v[122:125], v163 offset:16384
	ds_read_b128 v[158:161], v163 offset:32768
	ds_read_b128 v[170:173], v163 offset:49152
	s_waitcnt vmcnt(19) lgkmcnt(3)
	v_mfma_f32_16x16x32_f16 v[66:69], v[126:129], v[110:113], v[66:69]
	s_waitcnt vmcnt(18)
	v_mfma_f32_16x16x32_f16 v[70:73], v[174:177], v[110:113], v[70:73]
	s_waitcnt vmcnt(17)
	v_mfma_f32_16x16x32_f16 v[74:77], v[192:195], v[110:113], v[74:77]
	s_waitcnt vmcnt(16)
	v_mfma_f32_16x16x32_f16 v[110:113], v[196:199], v[110:113], v[18:21]
	s_waitcnt lgkmcnt(2)
	v_mfma_f32_16x16x32_f16 v[50:53], v[126:129], v[122:125], v[50:53]
	v_mfma_f32_16x16x32_f16 v[78:81], v[174:177], v[122:125], v[78:81]
	v_mfma_f32_16x16x32_f16 v[82:85], v[192:195], v[122:125], v[82:85]
	v_mfma_f32_16x16x32_f16 v[122:125], v[196:199], v[122:125], v[22:25]
	s_waitcnt lgkmcnt(1)
	v_mfma_f32_16x16x32_f16 v[216:219], v[126:129], v[158:161], v[54:57]
	v_mfma_f32_16x16x32_f16 v[86:89], v[174:177], v[158:161], v[86:89]
	v_mfma_f32_16x16x32_f16 v[90:93], v[192:195], v[158:161], v[90:93]
	v_mfma_f32_16x16x32_f16 v[158:161], v[196:199], v[158:161], v[26:29]
	s_waitcnt lgkmcnt(0)
	v_mfma_f32_16x16x32_f16 v[94:97], v[174:177], v[170:173], v[94:97]
	v_mfma_f32_16x16x32_f16 v[98:101], v[192:195], v[170:173], v[98:101]
	v_mfma_f32_16x16x32_f16 v[220:223], v[126:129], v[170:173], v[58:61]
	v_mfma_f32_16x16x32_f16 v[170:173], v[196:199], v[170:173], v[30:33]
	v_add_u32_e32 v18, 0x10000, v163
	v_add_u32_e32 v22, 0x14000, v163
	v_add_u32_e32 v26, 0x18000, v163
	v_add_u32_e32 v30, 0x1c000, v163
	ds_read_b128 v[18:21], v18
	ds_read_b128 v[22:25], v22
	ds_read_b128 v[26:29], v26
	ds_read_b128 v[30:33], v30
	s_waitcnt lgkmcnt(3)
	v_mfma_f32_16x16x32_f16 v[130:133], v[126:129], v[18:21], v[130:133]
	v_mfma_f32_16x16x32_f16 v[134:137], v[174:177], v[18:21], v[134:137]
	v_mfma_f32_16x16x32_f16 v[138:141], v[192:195], v[18:21], v[138:141]
	s_waitcnt lgkmcnt(2)
	v_mfma_f32_16x16x32_f16 v[114:117], v[126:129], v[22:25], v[114:117]
	v_mfma_f32_16x16x32_f16 v[142:145], v[174:177], v[22:25], v[142:145]
	v_mfma_f32_16x16x32_f16 v[146:149], v[192:195], v[22:25], v[146:149]
	s_waitcnt lgkmcnt(1)
	v_mfma_f32_16x16x32_f16 v[150:153], v[174:177], v[26:29], v[150:153]
	v_mfma_f32_16x16x32_f16 v[154:157], v[192:195], v[26:29], v[154:157]
	v_mfma_f32_16x16x32_f16 v[224:227], v[196:199], v[18:21], v[62:65]
	v_mfma_f32_16x16x32_f16 v[228:231], v[196:199], v[22:25], v[102:105]
	v_mfma_f32_16x16x32_f16 v[232:235], v[126:129], v[26:29], v[118:121]
	v_mfma_f32_16x16x32_f16 v[236:239], v[196:199], v[26:29], v[106:109]
	s_waitcnt lgkmcnt(0)
	v_mfma_f32_16x16x32_f16 v[240:243], v[126:129], v[30:33], v[34:37]
	v_mfma_f32_16x16x32_f16 v[174:177], v[174:177], v[30:33], v[38:41]
	v_mfma_f32_16x16x32_f16 v[192:195], v[192:195], v[30:33], v[42:45]
	v_mfma_f32_16x16x32_f16 v[196:199], v[196:199], v[30:33], v[46:49]
	s_or_b32 s52, s49, s24
	s_lshl_b32 s0, s52, 12
	v_lshl_add_u64 v[30:31], v[166:167], 0, s[0:1]
	global_load_dwordx4 v[18:21], v[30:31], off
	global_load_dwordx4 v[22:25], v[30:31], off offset:1024
	global_load_dwordx4 v[26:29], v[30:31], off offset:2048
	s_nop 0
	global_load_dwordx4 v[30:33], v[30:31], off offset:3072
	v_lshl_add_u32 v118, s25, 10, v191
	ds_read_b128 v[46:49], v118
	ds_read_b128 v[62:65], v118 offset:16384
	ds_read_b128 v[102:105], v118 offset:32768
	ds_read_b128 v[106:109], v118 offset:49152
	s_waitcnt vmcnt(19) lgkmcnt(3)
	v_mfma_f32_16x16x32_f16 v[34:37], v[200:203], v[46:49], v[66:69]
	s_waitcnt vmcnt(18)
	v_mfma_f32_16x16x32_f16 v[38:41], v[204:207], v[46:49], v[70:73]
	s_waitcnt vmcnt(17)
	v_mfma_f32_16x16x32_f16 v[42:45], v[208:211], v[46:49], v[74:77]
	s_waitcnt vmcnt(16)
	v_mfma_f32_16x16x32_f16 v[46:49], v[212:215], v[46:49], v[110:113]
	s_waitcnt lgkmcnt(2)
	v_mfma_f32_16x16x32_f16 v[50:53], v[200:203], v[62:65], v[50:53]
	v_mfma_f32_16x16x32_f16 v[54:57], v[204:207], v[62:65], v[78:81]
	v_mfma_f32_16x16x32_f16 v[58:61], v[208:211], v[62:65], v[82:85]
	v_mfma_f32_16x16x32_f16 v[62:65], v[212:215], v[62:65], v[122:125]
	s_waitcnt lgkmcnt(1)
	v_mfma_f32_16x16x32_f16 v[66:69], v[200:203], v[102:105], v[216:219]
	v_mfma_f32_16x16x32_f16 v[70:73], v[204:207], v[102:105], v[86:89]
	v_mfma_f32_16x16x32_f16 v[74:77], v[208:211], v[102:105], v[90:93]
	v_mfma_f32_16x16x32_f16 v[78:81], v[212:215], v[102:105], v[158:161]
	s_waitcnt lgkmcnt(0)
	v_mfma_f32_16x16x32_f16 v[82:85], v[200:203], v[106:109], v[220:223]
	v_mfma_f32_16x16x32_f16 v[86:89], v[204:207], v[106:109], v[94:97]
	v_mfma_f32_16x16x32_f16 v[90:93], v[208:211], v[106:109], v[98:101]
	v_mfma_f32_16x16x32_f16 v[94:97], v[212:215], v[106:109], v[170:173]
	s_nop 0
	v_add_u32_e32 v98, 0x10000, v118
	v_add_u32_e32 v99, 0x14000, v118
	ds_read_b128 v[110:113], v98
	ds_read_b128 v[126:129], v99
	v_add_u32_e32 v98, 0x18000, v118
	v_add_u32_e32 v99, 0x1c000, v118
	ds_read_b128 v[158:161], v98
	ds_read_b128 v[170:173], v99
	s_waitcnt lgkmcnt(3)
	v_mfma_f32_16x16x32_f16 v[98:101], v[200:203], v[110:113], v[130:133]
	v_mfma_f32_16x16x32_f16 v[102:105], v[204:207], v[110:113], v[134:137]
	v_mfma_f32_16x16x32_f16 v[106:109], v[208:211], v[110:113], v[138:141]
	v_mfma_f32_16x16x32_f16 v[110:113], v[212:215], v[110:113], v[224:227]
	s_waitcnt lgkmcnt(2)
	v_mfma_f32_16x16x32_f16 v[114:117], v[200:203], v[126:129], v[114:117]
	v_mfma_f32_16x16x32_f16 v[118:121], v[204:207], v[126:129], v[142:145]
	v_mfma_f32_16x16x32_f16 v[122:125], v[208:211], v[126:129], v[146:149]
	v_mfma_f32_16x16x32_f16 v[126:129], v[212:215], v[126:129], v[228:231]
	s_waitcnt lgkmcnt(1)
	v_mfma_f32_16x16x32_f16 v[130:133], v[200:203], v[158:161], v[232:235]
	v_mfma_f32_16x16x32_f16 v[134:137], v[204:207], v[158:161], v[150:153]
	v_mfma_f32_16x16x32_f16 v[138:141], v[208:211], v[158:161], v[154:157]
	v_mfma_f32_16x16x32_f16 v[142:145], v[212:215], v[158:161], v[236:239]
	s_waitcnt lgkmcnt(0)
	v_mfma_f32_16x16x32_f16 v[146:149], v[200:203], v[170:173], v[240:243]
	v_mfma_f32_16x16x32_f16 v[150:153], v[204:207], v[170:173], v[174:177]
	v_mfma_f32_16x16x32_f16 v[154:157], v[208:211], v[170:173], v[192:195]
	v_mfma_f32_16x16x32_f16 v[158:161], v[212:215], v[170:173], v[196:199]
	s_waitcnt vmcnt(0)
	s_barrier
	s_getreg_b32 s24, hwreg(HW_REG_XCC_ID, 0, 4)
	s_and_saveexec_b64 s[0:1], s[4:5]
	s_cbranch_execz .LBB5_145
	s_and_b32 s53, s24, 15
	s_lshl_b32 s24, s34, 3
	s_or_b32 s50, s24, s50
	s_or_b32 s24, s50, s58
	s_lshl_b32 s24, s24, 5
	s_ashr_i32 s25, s24, 31
	s_lshl_b64 s[24:25], s[24:25], 2
	s_add_u32 s24, s46, s24
	s_addc_u32 s25, s47, s25
	s_add_i32 s54, s53, 1
	v_mov_b32_e32 v163, s54
	s_or_b32 s24, s50, s2
	s_lshl_b32 s24, s24, 5
	s_ashr_i32 s25, s24, 31
	s_lshl_b64 s[24:25], s[24:25], 2
	s_add_u32 s24, s46, s24
	s_addc_u32 s25, s47, s25
	s_mov_b32 s90, 0
	v_mov_b32_e32 v163, v254
	v_cmp_ne_u32_e32 vcc, 0, v163
	s_cbranch_vccnz .LBB5_144
	s_mov_b32 s90, 2
	v_mov_b32_e32 v165, 0

.Lex_skip:
.LBB5_148:
	s_or_b32 s2, s49, s28
	s_lshl_b32 s0, s2, 12
	s_mov_b32 s1, 0
	v_lshl_add_u64 v[176:177], v[166:167], 0, s[0:1]
	s_waitcnt vmcnt(0)
	s_waitcnt vmcnt(0) lgkmcnt(0)
	s_barrier
	global_load_dwordx4 v[162:165], v[176:177], off
	global_load_dwordx4 v[168:171], v[176:177], off offset:1024
	global_load_dwordx4 v[172:175], v[176:177], off offset:2048
	s_nop 0
	global_load_dwordx4 v[176:179], v[176:177], off offset:3072
	v_lshl_add_u32 v208, s51, 10, v191
	ds_read_b128 v[192:195], v208
	ds_read_b128 v[196:199], v208 offset:16384
	ds_read_b128 v[200:203], v208 offset:32768
	ds_read_b128 v[204:207], v208 offset:49152
	s_waitcnt lgkmcnt(3)
	v_mfma_f32_16x16x32_f16 v[34:37], v[2:5], v[192:195], v[34:37]
	v_mfma_f32_16x16x32_f16 v[38:41], v[6:9], v[192:195], v[38:41]
	v_mfma_f32_16x16x32_f16 v[42:45], v[10:13], v[192:195], v[42:45]
	v_mfma_f32_16x16x32_f16 v[46:49], v[14:17], v[192:195], v[46:49]
	s_waitcnt lgkmcnt(2)
	v_mfma_f32_16x16x32_f16 v[50:53], v[2:5], v[196:199], v[50:53]
	v_mfma_f32_16x16x32_f16 v[54:57], v[6:9], v[196:199], v[54:57]
	v_mfma_f32_16x16x32_f16 v[58:61], v[10:13], v[196:199], v[58:61]
	v_mfma_f32_16x16x32_f16 v[62:65], v[14:17], v[196:199], v[62:65]
	s_waitcnt lgkmcnt(1)
	v_mfma_f32_16x16x32_f16 v[66:69], v[2:5], v[200:203], v[66:69]
	v_mfma_f32_16x16x32_f16 v[70:73], v[6:9], v[200:203], v[70:73]
	v_mfma_f32_16x16x32_f16 v[74:77], v[10:13], v[200:203], v[74:77]
	v_mfma_f32_16x16x32_f16 v[78:81], v[14:17], v[200:203], v[78:81]
	s_waitcnt lgkmcnt(0)
	v_mfma_f32_16x16x32_f16 v[82:85], v[2:5], v[204:207], v[82:85]
	v_mfma_f32_16x16x32_f16 v[86:89], v[6:9], v[204:207], v[86:89]
	v_mfma_f32_16x16x32_f16 v[90:93], v[10:13], v[204:207], v[90:93]
	v_mfma_f32_16x16x32_f16 v[94:97], v[14:17], v[204:207], v[94:97]
	v_add_u32_e32 v192, 0x10000, v208
	v_add_u32_e32 v196, 0x14000, v208
	v_add_u32_e32 v200, 0x18000, v208
	v_add_u32_e32 v204, 0x1c000, v208
	ds_read_b128 v[192:195], v192
	ds_read_b128 v[196:199], v196
	ds_read_b128 v[200:203], v200
	ds_read_b128 v[204:207], v204
	s_waitcnt lgkmcnt(3)
	v_mfma_f32_16x16x32_f16 v[98:101], v[2:5], v[192:195], v[98:101]
	v_mfma_f32_16x16x32_f16 v[102:105], v[6:9], v[192:195], v[102:105]
	v_mfma_f32_16x16x32_f16 v[106:109], v[10:13], v[192:195], v[106:109]
	v_mfma_f32_16x16x32_f16 v[110:113], v[14:17], v[192:195], v[110:113]
	s_waitcnt lgkmcnt(2)
	v_mfma_f32_16x16x32_f16 v[114:117], v[2:5], v[196:199], v[114:117]
	v_mfma_f32_16x16x32_f16 v[118:121], v[6:9], v[196:199], v[118:121]
	v_mfma_f32_16x16x32_f16 v[122:125], v[10:13], v[196:199], v[122:125]
	v_mfma_f32_16x16x32_f16 v[126:129], v[14:17], v[196:199], v[126:129]
	s_waitcnt lgkmcnt(1)
	v_mfma_f32_16x16x32_f16 v[130:133], v[2:5], v[200:203], v[130:133]
	v_mfma_f32_16x16x32_f16 v[134:137], v[6:9], v[200:203], v[134:137]
	v_mfma_f32_16x16x32_f16 v[138:141], v[10:13], v[200:203], v[138:141]
	v_mfma_f32_16x16x32_f16 v[142:145], v[14:17], v[200:203], v[142:145]
	s_waitcnt lgkmcnt(0)
	v_mfma_f32_16x16x32_f16 v[2:5], v[2:5], v[204:207], v[146:149]
	v_mfma_f32_16x16x32_f16 v[6:9], v[6:9], v[204:207], v[150:153]
	v_mfma_f32_16x16x32_f16 v[10:13], v[10:13], v[204:207], v[154:157]
	v_mfma_f32_16x16x32_f16 v[14:17], v[14:17], v[204:207], v[158:161]
	s_or_b32 s3, s49, s29
	s_lshl_b32 s0, s3, 12
	v_lshl_add_u64 v[158:159], v[166:167], 0, s[0:1]
	global_load_dwordx4 v[146:149], v[158:159], off
	global_load_dwordx4 v[150:153], v[158:159], off offset:1024
	global_load_dwordx4 v[154:157], v[158:159], off offset:2048
	s_nop 0
	global_load_dwordx4 v[158:161], v[158:159], off offset:3072
	v_lshl_add_u32 v208, s52, 10, v191
	ds_read_b128 v[192:195], v208
	ds_read_b128 v[196:199], v208 offset:16384
	ds_read_b128 v[200:203], v208 offset:32768
	ds_read_b128 v[204:207], v208 offset:49152
	s_waitcnt lgkmcnt(3)
	v_mfma_f32_16x16x32_f16 v[34:37], v[18:21], v[192:195], v[34:37]
	v_mfma_f32_16x16x32_f16 v[38:41], v[22:25], v[192:195], v[38:41]
	v_mfma_f32_16x16x32_f16 v[42:45], v[26:29], v[192:195], v[42:45]
	v_mfma_f32_16x16x32_f16 v[46:49], v[30:33], v[192:195], v[46:49]
	s_waitcnt lgkmcnt(2)
	v_mfma_f32_16x16x32_f16 v[50:53], v[18:21], v[196:199], v[50:53]
	v_mfma_f32_16x16x32_f16 v[54:57], v[22:25], v[196:199], v[54:57]
	v_mfma_f32_16x16x32_f16 v[58:61], v[26:29], v[196:199], v[58:61]
	v_mfma_f32_16x16x32_f16 v[62:65], v[30:33], v[196:199], v[62:65]
	s_waitcnt lgkmcnt(1)
	v_mfma_f32_16x16x32_f16 v[66:69], v[18:21], v[200:203], v[66:69]
	v_mfma_f32_16x16x32_f16 v[70:73], v[22:25], v[200:203], v[70:73]
	v_mfma_f32_16x16x32_f16 v[74:77], v[26:29], v[200:203], v[74:77]
	v_mfma_f32_16x16x32_f16 v[78:81], v[30:33], v[200:203], v[78:81]
	s_waitcnt lgkmcnt(0)
	v_mfma_f32_16x16x32_f16 v[82:85], v[18:21], v[204:207], v[82:85]
	v_mfma_f32_16x16x32_f16 v[86:89], v[22:25], v[204:207], v[86:89]
	v_mfma_f32_16x16x32_f16 v[90:93], v[26:29], v[204:207], v[90:93]
	v_mfma_f32_16x16x32_f16 v[94:97], v[30:33], v[204:207], v[94:97]
	v_add_u32_e32 v192, 0x10000, v208
	v_add_u32_e32 v196, 0x14000, v208
	v_add_u32_e32 v200, 0x18000, v208
	v_add_u32_e32 v204, 0x1c000, v208
	ds_read_b128 v[192:195], v192
	ds_read_b128 v[196:199], v196
	ds_read_b128 v[200:203], v200
	ds_read_b128 v[204:207], v204
	s_waitcnt lgkmcnt(3)
	v_mfma_f32_16x16x32_f16 v[98:101], v[18:21], v[192:195], v[98:101]
	v_mfma_f32_16x16x32_f16 v[102:105], v[22:25], v[192:195], v[102:105]
	v_mfma_f32_16x16x32_f16 v[106:109], v[26:29], v[192:195], v[106:109]
	v_mfma_f32_16x16x32_f16 v[110:113], v[30:33], v[192:195], v[110:113]
	s_waitcnt lgkmcnt(2)
	v_mfma_f32_16x16x32_f16 v[114:117], v[18:21], v[196:199], v[114:117]
	v_mfma_f32_16x16x32_f16 v[118:121], v[22:25], v[196:199], v[118:121]
	v_mfma_f32_16x16x32_f16 v[122:125], v[26:29], v[196:199], v[122:125]
	v_mfma_f32_16x16x32_f16 v[126:129], v[30:33], v[196:199], v[126:129]
	s_waitcnt lgkmcnt(1)
	v_mfma_f32_16x16x32_f16 v[130:133], v[18:21], v[200:203], v[130:133]
	v_mfma_f32_16x16x32_f16 v[134:137], v[22:25], v[200:203], v[134:137]
	v_mfma_f32_16x16x32_f16 v[138:141], v[26:29], v[200:203], v[138:141]
	s_waitcnt lgkmcnt(0)
	v_mfma_f32_16x16x32_f16 v[2:5], v[18:21], v[204:207], v[2:5]
	v_mfma_f32_16x16x32_f16 v[6:9], v[22:25], v[204:207], v[6:9]
	v_mfma_f32_16x16x32_f16 v[10:13], v[26:29], v[204:207], v[10:13]
	v_mfma_f32_16x16x32_f16 v[14:17], v[30:33], v[204:207], v[14:17]
	v_mfma_f32_16x16x32_f16 v[142:145], v[30:33], v[200:203], v[142:145]
	s_xor_b32 s7, s51, 4
	s_lshl_b32 s0, s7, 12
	v_lshl_add_u64 v[30:31], v[166:167], 0, s[0:1]
	global_load_dwordx4 v[18:21], v[30:31], off
	global_load_dwordx4 v[22:25], v[30:31], off offset:1024
	global_load_dwordx4 v[26:29], v[30:31], off offset:2048
	s_nop 0
	global_load_dwordx4 v[30:33], v[30:31], off offset:3072
	v_lshl_add_u32 v208, s2, 10, v191
	ds_read_b128 v[192:195], v208
	ds_read_b128 v[196:199], v208 offset:16384
	ds_read_b128 v[200:203], v208 offset:32768
	ds_read_b128 v[204:207], v208 offset:49152
	s_waitcnt vmcnt(11) lgkmcnt(3)
	v_mfma_f32_16x16x32_f16 v[34:37], v[162:165], v[192:195], v[34:37]
	s_waitcnt vmcnt(10)
	v_mfma_f32_16x16x32_f16 v[38:41], v[168:171], v[192:195], v[38:41]
	s_waitcnt vmcnt(9)
	v_mfma_f32_16x16x32_f16 v[42:45], v[172:175], v[192:195], v[42:45]
	s_waitcnt vmcnt(8)
	v_mfma_f32_16x16x32_f16 v[46:49], v[176:179], v[192:195], v[46:49]
	s_waitcnt lgkmcnt(2)
	v_mfma_f32_16x16x32_f16 v[50:53], v[162:165], v[196:199], v[50:53]
	v_mfma_f32_16x16x32_f16 v[54:57], v[168:171], v[196:199], v[54:57]
	v_mfma_f32_16x16x32_f16 v[58:61], v[172:175], v[196:199], v[58:61]
	v_mfma_f32_16x16x32_f16 v[62:65], v[176:179], v[196:199], v[62:65]
	s_waitcnt lgkmcnt(1)
	v_mfma_f32_16x16x32_f16 v[66:69], v[162:165], v[200:203], v[66:69]
	v_mfma_f32_16x16x32_f16 v[70:73], v[168:171], v[200:203], v[70:73]
	v_mfma_f32_16x16x32_f16 v[74:77], v[172:175], v[200:203], v[74:77]
	v_mfma_f32_16x16x32_f16 v[78:81], v[176:179], v[200:203], v[78:81]
	s_waitcnt lgkmcnt(0)
	v_mfma_f32_16x16x32_f16 v[82:85], v[162:165], v[204:207], v[82:85]
	v_mfma_f32_16x16x32_f16 v[86:89], v[168:171], v[204:207], v[86:89]
	v_mfma_f32_16x16x32_f16 v[90:93], v[172:175], v[204:207], v[90:93]
	v_mfma_f32_16x16x32_f16 v[94:97], v[176:179], v[204:207], v[94:97]
	v_add_u32_e32 v192, 0x10000, v208
	v_add_u32_e32 v196, 0x14000, v208
	v_add_u32_e32 v200, 0x18000, v208
	v_add_u32_e32 v204, 0x1c000, v208
	ds_read_b128 v[192:195], v192
	ds_read_b128 v[196:199], v196
	ds_read_b128 v[200:203], v200
	ds_read_b128 v[204:207], v204
	s_waitcnt lgkmcnt(3)
	v_mfma_f32_16x16x32_f16 v[98:101], v[162:165], v[192:195], v[98:101]
	v_mfma_f32_16x16x32_f16 v[102:105], v[168:171], v[192:195], v[102:105]
	v_mfma_f32_16x16x32_f16 v[106:109], v[172:175], v[192:195], v[106:109]
	v_mfma_f32_16x16x32_f16 v[110:113], v[176:179], v[192:195], v[110:113]
	s_waitcnt lgkmcnt(2)
	v_mfma_f32_16x16x32_f16 v[114:117], v[162:165], v[196:199], v[114:117]
	v_mfma_f32_16x16x32_f16 v[118:121], v[168:171], v[196:199], v[118:121]
	v_mfma_f32_16x16x32_f16 v[122:125], v[172:175], v[196:199], v[122:125]
	v_mfma_f32_16x16x32_f16 v[126:129], v[176:179], v[196:199], v[126:129]
	s_waitcnt lgkmcnt(1)
	v_mfma_f32_16x16x32_f16 v[130:133], v[162:165], v[200:203], v[130:133]
	v_mfma_f32_16x16x32_f16 v[134:137], v[168:171], v[200:203], v[134:137]
	v_mfma_f32_16x16x32_f16 v[138:141], v[172:175], v[200:203], v[138:141]
	s_waitcnt lgkmcnt(0)
	v_mfma_f32_16x16x32_f16 v[2:5], v[162:165], v[204:207], v[2:5]
	v_mfma_f32_16x16x32_f16 v[6:9], v[168:171], v[204:207], v[6:9]
	v_mfma_f32_16x16x32_f16 v[10:13], v[172:175], v[204:207], v[10:13]
	v_mfma_f32_16x16x32_f16 v[14:17], v[176:179], v[204:207], v[14:17]
	v_mfma_f32_16x16x32_f16 v[142:145], v[176:179], v[200:203], v[142:145]
	s_or_b32 s2, s49, s30
	s_lshl_b32 s0, s2, 12
	v_lshl_add_u64 v[176:177], v[166:167], 0, s[0:1]
	global_load_dwordx4 v[162:165], v[176:177], off
	global_load_dwordx4 v[168:171], v[176:177], off offset:1024
	global_load_dwordx4 v[172:175], v[176:177], off offset:2048
	s_nop 0
	global_load_dwordx4 v[176:179], v[176:177], off offset:3072
	v_lshl_add_u32 v208, s3, 10, v191
	ds_read_b128 v[192:195], v208
	ds_read_b128 v[196:199], v208 offset:16384
	ds_read_b128 v[200:203], v208 offset:32768
	ds_read_b128 v[204:207], v208 offset:49152
	s_waitcnt vmcnt(11) lgkmcnt(3)
	v_mfma_f32_16x16x32_f16 v[34:37], v[146:149], v[192:195], v[34:37]
	s_waitcnt vmcnt(10)
	v_mfma_f32_16x16x32_f16 v[38:41], v[150:153], v[192:195], v[38:41]
	s_waitcnt vmcnt(9)
	v_mfma_f32_16x16x32_f16 v[42:45], v[154:157], v[192:195], v[42:45]
	s_waitcnt vmcnt(8)
	v_mfma_f32_16x16x32_f16 v[46:49], v[158:161], v[192:195], v[46:49]
	s_waitcnt lgkmcnt(2)
	v_mfma_f32_16x16x32_f16 v[50:53], v[146:149], v[196:199], v[50:53]
	v_mfma_f32_16x16x32_f16 v[54:57], v[150:153], v[196:199], v[54:57]
	v_mfma_f32_16x16x32_f16 v[58:61], v[154:157], v[196:199], v[58:61]
	v_mfma_f32_16x16x32_f16 v[62:65], v[158:161], v[196:199], v[62:65]
	s_waitcnt lgkmcnt(1)
	v_mfma_f32_16x16x32_f16 v[66:69], v[146:149], v[200:203], v[66:69]
	v_mfma_f32_16x16x32_f16 v[70:73], v[150:153], v[200:203], v[70:73]
	v_mfma_f32_16x16x32_f16 v[74:77], v[154:157], v[200:203], v[74:77]
	v_mfma_f32_16x16x32_f16 v[78:81], v[158:161], v[200:203], v[78:81]
	s_waitcnt lgkmcnt(0)
	v_mfma_f32_16x16x32_f16 v[82:85], v[146:149], v[204:207], v[82:85]
	v_mfma_f32_16x16x32_f16 v[86:89], v[150:153], v[204:207], v[86:89]
	v_mfma_f32_16x16x32_f16 v[90:93], v[154:157], v[204:207], v[90:93]
	v_mfma_f32_16x16x32_f16 v[94:97], v[158:161], v[204:207], v[94:97]
	v_add_u32_e32 v192, 0x10000, v208
	v_add_u32_e32 v196, 0x14000, v208
	v_add_u32_e32 v200, 0x18000, v208
	v_add_u32_e32 v204, 0x1c000, v208
	ds_read_b128 v[192:195], v192
	ds_read_b128 v[196:199], v196
	ds_read_b128 v[200:203], v200
	ds_read_b128 v[204:207], v204
	s_waitcnt lgkmcnt(3)
	v_mfma_f32_16x16x32_f16 v[98:101], v[146:149], v[192:195], v[98:101]
	v_mfma_f32_16x16x32_f16 v[102:105], v[150:153], v[192:195], v[102:105]
	v_mfma_f32_16x16x32_f16 v[106:109], v[154:157], v[192:195], v[106:109]
	v_mfma_f32_16x16x32_f16 v[110:113], v[158:161], v[192:195], v[110:113]
	s_waitcnt lgkmcnt(2)
	v_mfma_f32_16x16x32_f16 v[114:117], v[146:149], v[196:199], v[114:117]
	v_mfma_f32_16x16x32_f16 v[118:121], v[150:153], v[196:199], v[118:121]
	v_mfma_f32_16x16x32_f16 v[122:125], v[154:157], v[196:199], v[122:125]
	v_mfma_f32_16x16x32_f16 v[126:129], v[158:161], v[196:199], v[126:129]
	s_waitcnt lgkmcnt(1)
	v_mfma_f32_16x16x32_f16 v[130:133], v[146:149], v[200:203], v[130:133]
	v_mfma_f32_16x16x32_f16 v[134:137], v[150:153], v[200:203], v[134:137]
	v_mfma_f32_16x16x32_f16 v[138:141], v[154:157], v[200:203], v[138:141]
	s_waitcnt lgkmcnt(0)
	v_mfma_f32_16x16x32_f16 v[2:5], v[146:149], v[204:207], v[2:5]
	v_mfma_f32_16x16x32_f16 v[6:9], v[150:153], v[204:207], v[6:9]
	v_mfma_f32_16x16x32_f16 v[10:13], v[154:157], v[204:207], v[10:13]
	v_mfma_f32_16x16x32_f16 v[14:17], v[158:161], v[204:207], v[14:17]
	v_mfma_f32_16x16x32_f16 v[142:145], v[158:161], v[200:203], v[142:145]
	s_or_b32 s3, s49, s31
	s_lshl_b32 s0, s3, 12
	v_lshl_add_u64 v[158:159], v[166:167], 0, s[0:1]
	global_load_dwordx4 v[146:149], v[158:159], off
	global_load_dwordx4 v[150:153], v[158:159], off offset:1024
	global_load_dwordx4 v[154:157], v[158:159], off offset:2048
	s_nop 0
	global_load_dwordx4 v[158:161], v[158:159], off offset:3072
	v_lshl_add_u32 v208, s7, 10, v191
	ds_read_b128 v[192:195], v208
	ds_read_b128 v[196:199], v208 offset:16384
	ds_read_b128 v[200:203], v208 offset:32768
	ds_read_b128 v[204:207], v208 offset:49152
	s_waitcnt vmcnt(11) lgkmcnt(3)
	v_mfma_f32_16x16x32_f16 v[34:37], v[18:21], v[192:195], v[34:37]
	s_waitcnt vmcnt(10)
	v_mfma_f32_16x16x32_f16 v[38:41], v[22:25], v[192:195], v[38:41]
	s_waitcnt vmcnt(9)
	v_mfma_f32_16x16x32_f16 v[42:45], v[26:29], v[192:195], v[42:45]
	s_waitcnt vmcnt(8)
	v_mfma_f32_16x16x32_f16 v[46:49], v[30:33], v[192:195], v[46:49]
	s_waitcnt lgkmcnt(2)
	v_mfma_f32_16x16x32_f16 v[50:53], v[18:21], v[196:199], v[50:53]
	v_mfma_f32_16x16x32_f16 v[54:57], v[22:25], v[196:199], v[54:57]
	v_mfma_f32_16x16x32_f16 v[58:61], v[26:29], v[196:199], v[58:61]
	v_mfma_f32_16x16x32_f16 v[62:65], v[30:33], v[196:199], v[62:65]
	s_waitcnt lgkmcnt(1)
	v_mfma_f32_16x16x32_f16 v[66:69], v[18:21], v[200:203], v[66:69]
	v_mfma_f32_16x16x32_f16 v[70:73], v[22:25], v[200:203], v[70:73]
	v_mfma_f32_16x16x32_f16 v[74:77], v[26:29], v[200:203], v[74:77]
	v_mfma_f32_16x16x32_f16 v[78:81], v[30:33], v[200:203], v[78:81]
	s_waitcnt lgkmcnt(0)
	v_mfma_f32_16x16x32_f16 v[82:85], v[18:21], v[204:207], v[82:85]
	v_mfma_f32_16x16x32_f16 v[86:89], v[22:25], v[204:207], v[86:89]
	v_mfma_f32_16x16x32_f16 v[90:93], v[26:29], v[204:207], v[90:93]
	v_mfma_f32_16x16x32_f16 v[94:97], v[30:33], v[204:207], v[94:97]
	v_add_u32_e32 v192, 0x10000, v208
	v_add_u32_e32 v196, 0x14000, v208
	v_add_u32_e32 v200, 0x18000, v208
	v_add_u32_e32 v204, 0x1c000, v208
	ds_read_b128 v[192:195], v192
	ds_read_b128 v[196:199], v196
	ds_read_b128 v[200:203], v200
	ds_read_b128 v[204:207], v204
	s_waitcnt lgkmcnt(3)
	v_mfma_f32_16x16x32_f16 v[98:101], v[18:21], v[192:195], v[98:101]
	v_mfma_f32_16x16x32_f16 v[102:105], v[22:25], v[192:195], v[102:105]
	v_mfma_f32_16x16x32_f16 v[106:109], v[26:29], v[192:195], v[106:109]
	v_mfma_f32_16x16x32_f16 v[110:113], v[30:33], v[192:195], v[110:113]
	s_waitcnt lgkmcnt(2)
	v_mfma_f32_16x16x32_f16 v[114:117], v[18:21], v[196:199], v[114:117]
	v_mfma_f32_16x16x32_f16 v[118:121], v[22:25], v[196:199], v[118:121]
	v_mfma_f32_16x16x32_f16 v[122:125], v[26:29], v[196:199], v[122:125]
	v_mfma_f32_16x16x32_f16 v[126:129], v[30:33], v[196:199], v[126:129]
	s_waitcnt lgkmcnt(1)
	v_mfma_f32_16x16x32_f16 v[130:133], v[18:21], v[200:203], v[130:133]
	v_mfma_f32_16x16x32_f16 v[134:137], v[22:25], v[200:203], v[134:137]
	v_mfma_f32_16x16x32_f16 v[138:141], v[26:29], v[200:203], v[138:141]
	s_waitcnt lgkmcnt(0)
	v_mfma_f32_16x16x32_f16 v[2:5], v[18:21], v[204:207], v[2:5]
	v_mfma_f32_16x16x32_f16 v[6:9], v[22:25], v[204:207], v[6:9]
	v_mfma_f32_16x16x32_f16 v[10:13], v[26:29], v[204:207], v[10:13]
	v_mfma_f32_16x16x32_f16 v[14:17], v[30:33], v[204:207], v[14:17]
	v_mfma_f32_16x16x32_f16 v[142:145], v[30:33], v[200:203], v[142:145]
	s_or_b32 s7, s49, s48
	s_lshl_b32 s0, s7, 12
	v_lshl_add_u64 v[26:27], v[166:167], 0, s[0:1]
	global_load_dwordx4 v[18:21], v[26:27], off
	global_load_dwordx4 v[22:25], v[26:27], off offset:1024
	global_load_dwordx4 v[30:33], v[26:27], off offset:2048
	global_load_dwordx4 v[192:195], v[26:27], off offset:3072
	v_lshl_add_u32 v166, s2, 10, v191
	ds_read_b128 v[26:29], v166
	ds_read_b128 v[196:199], v166 offset:16384
	ds_read_b128 v[200:203], v166 offset:32768
	ds_read_b128 v[204:207], v166 offset:49152
	s_waitcnt vmcnt(11) lgkmcnt(3)
	v_mfma_f32_16x16x32_f16 v[34:37], v[162:165], v[26:29], v[34:37]
	s_waitcnt vmcnt(10)
	v_mfma_f32_16x16x32_f16 v[38:41], v[168:171], v[26:29], v[38:41]
	s_waitcnt vmcnt(9)
	v_mfma_f32_16x16x32_f16 v[42:45], v[172:175], v[26:29], v[42:45]
	s_waitcnt vmcnt(8)
	v_mfma_f32_16x16x32_f16 v[26:29], v[176:179], v[26:29], v[46:49]
	s_waitcnt lgkmcnt(2)
	v_mfma_f32_16x16x32_f16 v[46:49], v[162:165], v[196:199], v[50:53]
	v_mfma_f32_16x16x32_f16 v[50:53], v[168:171], v[196:199], v[54:57]
	v_mfma_f32_16x16x32_f16 v[54:57], v[172:175], v[196:199], v[58:61]
	v_mfma_f32_16x16x32_f16 v[58:61], v[176:179], v[196:199], v[62:65]
	s_waitcnt lgkmcnt(1)
	v_mfma_f32_16x16x32_f16 v[62:65], v[162:165], v[200:203], v[66:69]
	v_mfma_f32_16x16x32_f16 v[66:69], v[168:171], v[200:203], v[70:73]
	v_mfma_f32_16x16x32_f16 v[70:73], v[172:175], v[200:203], v[74:77]
	v_mfma_f32_16x16x32_f16 v[74:77], v[176:179], v[200:203], v[78:81]
	s_waitcnt lgkmcnt(0)
	v_mfma_f32_16x16x32_f16 v[78:81], v[162:165], v[204:207], v[82:85]
	v_mfma_f32_16x16x32_f16 v[82:85], v[168:171], v[204:207], v[86:89]
	v_mfma_f32_16x16x32_f16 v[86:89], v[172:175], v[204:207], v[90:93]
	v_mfma_f32_16x16x32_f16 v[90:93], v[176:179], v[204:207], v[94:97]
	s_nop 1
	v_add_u32_e32 v94, 0x10000, v166
	v_add_u32_e32 v167, 0x14000, v166
	ds_read_b128 v[94:97], v94
	ds_read_b128 v[196:199], v167
	v_add_u32_e32 v167, 0x18000, v166
	v_add_u32_e32 v166, 0x1c000, v166
	ds_read_b128 v[200:203], v167
	ds_read_b128 v[204:207], v166
	s_waitcnt lgkmcnt(3)
	v_mfma_f32_16x16x32_f16 v[98:101], v[162:165], v[94:97], v[98:101]
	v_mfma_f32_16x16x32_f16 v[102:105], v[168:171], v[94:97], v[102:105]
	v_mfma_f32_16x16x32_f16 v[106:109], v[172:175], v[94:97], v[106:109]
	v_mfma_f32_16x16x32_f16 v[94:97], v[176:179], v[94:97], v[110:113]
	s_waitcnt lgkmcnt(2)
	v_mfma_f32_16x16x32_f16 v[110:113], v[162:165], v[196:199], v[114:117]
	v_mfma_f32_16x16x32_f16 v[114:117], v[168:171], v[196:199], v[118:121]
	v_mfma_f32_16x16x32_f16 v[118:121], v[172:175], v[196:199], v[122:125]
	v_mfma_f32_16x16x32_f16 v[122:125], v[176:179], v[196:199], v[126:129]
	s_waitcnt lgkmcnt(1)
	v_mfma_f32_16x16x32_f16 v[126:129], v[162:165], v[200:203], v[130:133]
	v_mfma_f32_16x16x32_f16 v[130:133], v[168:171], v[200:203], v[134:137]
	v_mfma_f32_16x16x32_f16 v[134:137], v[172:175], v[200:203], v[138:141]
	v_mfma_f32_16x16x32_f16 v[138:141], v[176:179], v[200:203], v[142:145]
	s_waitcnt lgkmcnt(0)
	v_mfma_f32_16x16x32_f16 v[2:5], v[162:165], v[204:207], v[2:5]
	v_mfma_f32_16x16x32_f16 v[6:9], v[168:171], v[204:207], v[6:9]
	v_mfma_f32_16x16x32_f16 v[10:13], v[172:175], v[204:207], v[10:13]
	v_mfma_f32_16x16x32_f16 v[14:17], v[176:179], v[204:207], v[14:17]
	v_lshl_add_u32 v174, s3, 10, v191
	ds_read_b128 v[142:145], v174
	ds_read_b128 v[162:165], v174 offset:16384
	ds_read_b128 v[166:169], v174 offset:32768
	ds_read_b128 v[170:173], v174 offset:49152
	s_waitcnt vmcnt(7) lgkmcnt(3)
	v_mfma_f32_16x16x32_f16 v[34:37], v[146:149], v[142:145], v[34:37]
	s_waitcnt vmcnt(6)
	v_mfma_f32_16x16x32_f16 v[38:41], v[150:153], v[142:145], v[38:41]
	s_waitcnt vmcnt(5)
	v_mfma_f32_16x16x32_f16 v[42:45], v[154:157], v[142:145], v[42:45]
	s_waitcnt vmcnt(4)
	v_mfma_f32_16x16x32_f16 v[26:29], v[158:161], v[142:145], v[26:29]
	s_waitcnt lgkmcnt(2)
	v_mfma_f32_16x16x32_f16 v[46:49], v[146:149], v[162:165], v[46:49]
	v_mfma_f32_16x16x32_f16 v[50:53], v[150:153], v[162:165], v[50:53]
	v_mfma_f32_16x16x32_f16 v[54:57], v[154:157], v[162:165], v[54:57]
	v_mfma_f32_16x16x32_f16 v[58:61], v[158:161], v[162:165], v[58:61]
	s_waitcnt lgkmcnt(1)
	v_mfma_f32_16x16x32_f16 v[62:65], v[146:149], v[166:169], v[62:65]
	v_mfma_f32_16x16x32_f16 v[66:69], v[150:153], v[166:169], v[66:69]
	v_mfma_f32_16x16x32_f16 v[70:73], v[154:157], v[166:169], v[70:73]
	v_mfma_f32_16x16x32_f16 v[74:77], v[158:161], v[166:169], v[74:77]
	s_waitcnt lgkmcnt(0)
	v_mfma_f32_16x16x32_f16 v[78:81], v[146:149], v[170:173], v[78:81]
	v_mfma_f32_16x16x32_f16 v[82:85], v[150:153], v[170:173], v[82:85]
	v_mfma_f32_16x16x32_f16 v[86:89], v[154:157], v[170:173], v[86:89]
	v_mfma_f32_16x16x32_f16 v[162:165], v[158:161], v[170:173], v[90:93]
	s_nop 1
	v_add_u32_e32 v90, 0x10000, v174
	v_add_u32_e32 v142, 0x14000, v174
	v_add_u32_e32 v166, 0x18000, v174
	v_add_u32_e32 v170, 0x1c000, v174
	ds_read_b128 v[90:93], v90
	ds_read_b128 v[142:145], v142
	ds_read_b128 v[166:169], v166
	ds_read_b128 v[170:173], v170
	s_waitcnt lgkmcnt(0)
	v_mfma_f32_16x16x32_f16 v[2:5], v[146:149], v[170:173], v[2:5]
	v_mfma_f32_16x16x32_f16 v[6:9], v[150:153], v[170:173], v[6:9]
	v_mfma_f32_16x16x32_f16 v[10:13], v[154:157], v[170:173], v[10:13]
	v_mfma_f32_16x16x32_f16 v[14:17], v[158:161], v[170:173], v[14:17]
	v_mfma_f32_16x16x32_f16 v[174:177], v[146:149], v[90:93], v[98:101]
	v_mfma_f32_16x16x32_f16 v[196:199], v[150:153], v[90:93], v[102:105]
	v_mfma_f32_16x16x32_f16 v[200:203], v[154:157], v[90:93], v[106:109]
	v_mfma_f32_16x16x32_f16 v[204:207], v[158:161], v[90:93], v[94:97]
	v_mfma_f32_16x16x32_f16 v[208:211], v[146:149], v[142:145], v[110:113]
	v_mfma_f32_16x16x32_f16 v[212:215], v[150:153], v[142:145], v[114:117]
	v_mfma_f32_16x16x32_f16 v[216:219], v[154:157], v[142:145], v[118:121]
	v_mfma_f32_16x16x32_f16 v[220:223], v[158:161], v[142:145], v[122:125]
	v_mfma_f32_16x16x32_f16 v[224:227], v[146:149], v[166:169], v[126:129]
	v_mfma_f32_16x16x32_f16 v[228:231], v[150:153], v[166:169], v[130:133]
	v_mfma_f32_16x16x32_f16 v[232:235], v[154:157], v[166:169], v[134:137]
	v_mfma_f32_16x16x32_f16 v[166:169], v[158:161], v[166:169], v[138:141]
	v_lshl_add_u32 v158, s7, 10, v191
	ds_read_b128 v[90:93], v158
	ds_read_b128 v[94:97], v158 offset:16384
	ds_read_b128 v[98:101], v158 offset:32768
	ds_read_b128 v[146:149], v158 offset:49152
	s_waitcnt vmcnt(3) lgkmcnt(3)
	v_mfma_f32_16x16x32_f16 v[150:153], v[18:21], v[90:93], v[34:37]
	s_waitcnt vmcnt(2)
	v_mfma_f32_16x16x32_f16 v[138:141], v[22:25], v[90:93], v[38:41]
	s_waitcnt vmcnt(1)
	v_mfma_f32_16x16x32_f16 v[154:157], v[30:33], v[90:93], v[42:45]
	s_waitcnt vmcnt(0)
	v_mfma_f32_16x16x32_f16 v[142:145], v[192:195], v[90:93], v[26:29]
	s_waitcnt lgkmcnt(2)
	v_mfma_f32_16x16x32_f16 v[134:137], v[18:21], v[94:97], v[46:49]
	v_mfma_f32_16x16x32_f16 v[122:125], v[22:25], v[94:97], v[50:53]
	v_mfma_f32_16x16x32_f16 v[130:133], v[30:33], v[94:97], v[54:57]
	v_mfma_f32_16x16x32_f16 v[126:129], v[192:195], v[94:97], v[58:61]
	s_waitcnt lgkmcnt(1)
	v_mfma_f32_16x16x32_f16 v[118:121], v[18:21], v[98:101], v[62:65]
	v_mfma_f32_16x16x32_f16 v[106:109], v[22:25], v[98:101], v[66:69]
	v_mfma_f32_16x16x32_f16 v[114:117], v[30:33], v[98:101], v[70:73]
	v_mfma_f32_16x16x32_f16 v[110:113], v[192:195], v[98:101], v[74:77]
	s_waitcnt lgkmcnt(0)
	v_mfma_f32_16x16x32_f16 v[102:105], v[18:21], v[146:149], v[78:81]
	v_mfma_f32_16x16x32_f16 v[90:93], v[22:25], v[146:149], v[82:85]
	v_mfma_f32_16x16x32_f16 v[98:101], v[30:33], v[146:149], v[86:89]
	v_mfma_f32_16x16x32_f16 v[94:97], v[192:195], v[146:149], v[162:165]
	v_add_u32_e32 v26, 0x10000, v158
	v_add_u32_e32 v34, 0x14000, v158
	v_add_u32_e32 v38, 0x18000, v158
	ds_read_b128 v[26:29], v26
	ds_read_b128 v[34:37], v34
	v_add_u32_e32 v42, 0x1c000, v158
	ds_read_b128 v[38:41], v38
	ds_read_b128 v[146:149], v42
	s_waitcnt lgkmcnt(3)
	v_mfma_f32_16x16x32_f16 v[86:89], v[18:21], v[26:29], v[174:177]
	v_mfma_f32_16x16x32_f16 v[74:77], v[22:25], v[26:29], v[196:199]
	v_mfma_f32_16x16x32_f16 v[82:85], v[30:33], v[26:29], v[200:203]
	v_mfma_f32_16x16x32_f16 v[78:81], v[192:195], v[26:29], v[204:207]
	s_waitcnt lgkmcnt(2)
	v_mfma_f32_16x16x32_f16 v[70:73], v[18:21], v[34:37], v[208:211]
	v_mfma_f32_16x16x32_f16 v[58:61], v[22:25], v[34:37], v[212:215]
	v_mfma_f32_16x16x32_f16 v[66:69], v[30:33], v[34:37], v[216:219]
	v_mfma_f32_16x16x32_f16 v[62:65], v[192:195], v[34:37], v[220:223]
	s_waitcnt lgkmcnt(1)
	v_mfma_f32_16x16x32_f16 v[54:57], v[18:21], v[38:41], v[224:227]
	v_mfma_f32_16x16x32_f16 v[42:45], v[22:25], v[38:41], v[228:231]
	v_mfma_f32_16x16x32_f16 v[50:53], v[30:33], v[38:41], v[232:235]
	v_mfma_f32_16x16x32_f16 v[46:49], v[192:195], v[38:41], v[166:169]
	s_waitcnt lgkmcnt(0)
	v_mfma_f32_16x16x32_f16 v[26:29], v[18:21], v[146:149], v[2:5]
	v_mfma_f32_16x16x32_f16 v[2:5], v[22:25], v[146:149], v[6:9]
	v_mfma_f32_16x16x32_f16 v[22:25], v[30:33], v[146:149], v[10:13]
	v_mfma_f32_16x16x32_f16 v[6:9], v[192:195], v[146:149], v[14:17]
	s_lshl_b64 s[0:1], s[42:43], 2
	s_add_u32 s0, s18, s0
	s_addc_u32 s1, s19, s1
	s_lshl_b32 s2, s42, 8
	s_ashr_i32 s3, s2, 31
	v_lshlrev_b32_e32 v146, 5, v187
	s_lshl_b64 s[2:3], s[2:3], 2
	v_and_or_b32 v10, v190, 12, v146
	s_add_u32 s12, s12, s2
	s_addc_u32 s13, s13, s3
	v_lshlrev_b32_e32 v10, 2, v10
	v_add_u32_e32 v254, 0x22640, v10
	ds_read_b128 v[34:37], v254
	ds_read_b128 v[14:17], v254 offset:64
	ds_read_b128 v[38:41], v254 offset:1024
	ds_read_b128 v[18:21], v254 offset:1088
	ds_read_b128 v[30:33], v254 offset:2048
	ds_read_b128 v[10:13], v254 offset:2112
	s_add_u32 s12, s14, s2
	s_addc_u32 s13, s15, s3
	s_add_u32 s2, s16, s2
	s_addc_u32 s3, s17, s3
	s_nop 0
	v_cmp_gt_u32_e32 vcc, 16, v189
	s_mov_b32 s2, s69
	v_mov_b32_e32 v216, 0x3d38aa3b
	v_mov_b32_e32 v217, 0x3d38aa3b
	v_mov_b32_e32 v218, 0xbcb8aa3b
	v_mov_b32_e32 v219, 0xbcb8aa3b
	v_mov_b32_e32 v222, 1.0
	v_mov_b32_e32 v223, 1.0
	v_mov_b32_e32 v224, 0x4038aa3b
	v_mov_b32_e32 v225, 0x4038aa3b
	v_mov_b32_e32 v226, 0xbfb8aa3b
	v_mov_b32_e32 v227, 0xbfb8aa3b
	v_lshlrev_b32_e32 v232, 9, v187
	v_lshlrev_b32_e32 v233, 2, v188
	v_add3_u32 v232, s24, v232, v233
	s_waitcnt vmcnt(0) lgkmcnt(0)
	v_pk_mul_f32 v[34:35], v[34:35], v[224:225]
	v_pk_mul_f32 v[36:37], v[36:37], v[224:225]
	v_pk_mul_f32 v[14:15], v[14:15], v[224:225]
	v_pk_mul_f32 v[16:17], v[16:17], v[224:225]
	v_pk_mul_f32 v[38:39], v[38:39], v[226:227]
	v_pk_mul_f32 v[40:41], v[40:41], v[226:227]
	v_pk_mul_f32 v[18:19], v[18:19], v[226:227]
	v_pk_mul_f32 v[20:21], v[20:21], v[226:227]
	v_pk_fma_f32 v[150:151], v[150:151], v[216:217], v[34:35]
	v_pk_fma_f32 v[154:155], v[154:155], v[218:219], v[38:39]
	v_min_f32_e32 v150, 0x42700000, v150
	v_min_f32_e32 v151, 0x42700000, v151
	v_min_f32_e32 v154, 0x42700000, v154
	v_min_f32_e32 v155, 0x42700000, v155
	v_pk_fma_f32 v[152:153], v[152:153], v[216:217], v[36:37]
	v_pk_fma_f32 v[156:157], v[156:157], v[218:219], v[40:41]
	v_min_f32_e32 v152, 0x42700000, v152
	v_min_f32_e32 v153, 0x42700000, v153
	v_min_f32_e32 v156, 0x42700000, v156
	v_min_f32_e32 v157, 0x42700000, v157
	v_exp_f32_e32 v150, v150
	v_exp_f32_e32 v151, v151
	v_exp_f32_e32 v154, v154
	v_exp_f32_e32 v155, v155
	v_exp_f32_e32 v152, v152
	v_exp_f32_e32 v153, v153
	v_exp_f32_e32 v156, v156
	v_exp_f32_e32 v157, v157
	v_pk_fma_f32 v[228:229], v[150:151], v[30:31], v[30:31] neg_lo:[0,0,1] neg_hi:[0,0,1]
	v_pk_add_f32 v[154:155], v[154:155], v[222:223]
	v_pk_fma_f32 v[150:151], v[150:151], v[154:155], v[154:155]
	v_pk_fma_f32 v[230:231], v[152:153], v[32:33], v[32:33] neg_lo:[0,0,1] neg_hi:[0,0,1]
	v_pk_add_f32 v[156:157], v[156:157], v[222:223]
	v_pk_fma_f32 v[152:153], v[152:153], v[156:157], v[156:157]
	v_rcp_f32_e32 v150, v150
	v_rcp_f32_e32 v151, v151
	v_rcp_f32_e32 v152, v152
	v_rcp_f32_e32 v153, v153
	v_pk_mul_f32 v[200:201], v[228:229], v[150:151]
	v_pk_fma_f32 v[200:201], v[230:231], v[152:153], v[200:201]
	v_pk_fma_f32 v[138:139], v[138:139], v[216:217], v[14:15]
	v_pk_fma_f32 v[142:143], v[142:143], v[218:219], v[18:19]
	v_min_f32_e32 v138, 0x42700000, v138
	v_min_f32_e32 v139, 0x42700000, v139
	v_min_f32_e32 v142, 0x42700000, v142
	v_min_f32_e32 v143, 0x42700000, v143
	v_pk_fma_f32 v[140:141], v[140:141], v[216:217], v[16:17]
	v_pk_fma_f32 v[144:145], v[144:145], v[218:219], v[20:21]
	v_min_f32_e32 v140, 0x42700000, v140
	v_min_f32_e32 v141, 0x42700000, v141
	v_min_f32_e32 v144, 0x42700000, v144
	v_min_f32_e32 v145, 0x42700000, v145
	v_exp_f32_e32 v138, v138
	v_exp_f32_e32 v139, v139
	v_exp_f32_e32 v142, v142
	v_exp_f32_e32 v143, v143
	v_exp_f32_e32 v140, v140
	v_exp_f32_e32 v141, v141
	v_exp_f32_e32 v144, v144
	v_exp_f32_e32 v145, v145
	v_pk_fma_f32 v[228:229], v[138:139], v[10:11], v[10:11] neg_lo:[0,0,1] neg_hi:[0,0,1]
	v_pk_add_f32 v[142:143], v[142:143], v[222:223]
	v_pk_fma_f32 v[138:139], v[138:139], v[142:143], v[142:143]
	v_pk_fma_f32 v[230:231], v[140:141], v[12:13], v[12:13] neg_lo:[0,0,1] neg_hi:[0,0,1]
	v_pk_add_f32 v[144:145], v[144:145], v[222:223]
	v_pk_fma_f32 v[140:141], v[140:141], v[144:145], v[144:145]
	v_rcp_f32_e32 v138, v138
	v_rcp_f32_e32 v139, v139
	v_rcp_f32_e32 v140, v140
	v_rcp_f32_e32 v141, v141
	v_pk_fma_f32 v[200:201], v[228:229], v[138:139], v[200:201]
	v_pk_fma_f32 v[200:201], v[230:231], v[140:141], v[200:201]
	v_pk_fma_f32 v[134:135], v[134:135], v[216:217], v[34:35]
	v_pk_fma_f32 v[130:131], v[130:131], v[218:219], v[38:39]
	v_min_f32_e32 v134, 0x42700000, v134
	v_min_f32_e32 v135, 0x42700000, v135
	v_min_f32_e32 v130, 0x42700000, v130
	v_min_f32_e32 v131, 0x42700000, v131
	v_pk_fma_f32 v[136:137], v[136:137], v[216:217], v[36:37]
	v_pk_fma_f32 v[132:133], v[132:133], v[218:219], v[40:41]
	v_min_f32_e32 v136, 0x42700000, v136
	v_min_f32_e32 v137, 0x42700000, v137
	v_min_f32_e32 v132, 0x42700000, v132
	v_min_f32_e32 v133, 0x42700000, v133
	v_exp_f32_e32 v134, v134
	v_exp_f32_e32 v135, v135
	v_exp_f32_e32 v130, v130
	v_exp_f32_e32 v131, v131
	v_exp_f32_e32 v136, v136
	v_exp_f32_e32 v137, v137
	v_exp_f32_e32 v132, v132
	v_exp_f32_e32 v133, v133
	v_pk_fma_f32 v[228:229], v[134:135], v[30:31], v[30:31] neg_lo:[0,0,1] neg_hi:[0,0,1]
	v_pk_add_f32 v[130:131], v[130:131], v[222:223]
	v_pk_fma_f32 v[134:135], v[134:135], v[130:131], v[130:131]
	v_pk_fma_f32 v[230:231], v[136:137], v[32:33], v[32:33] neg_lo:[0,0,1] neg_hi:[0,0,1]
	v_pk_add_f32 v[132:133], v[132:133], v[222:223]
	v_pk_fma_f32 v[136:137], v[136:137], v[132:133], v[132:133]
	v_rcp_f32_e32 v134, v134
	v_rcp_f32_e32 v135, v135
	v_rcp_f32_e32 v136, v136
	v_rcp_f32_e32 v137, v137
	v_pk_mul_f32 v[202:203], v[228:229], v[134:135]
	v_pk_fma_f32 v[202:203], v[230:231], v[136:137], v[202:203]
	v_pk_fma_f32 v[122:123], v[122:123], v[216:217], v[14:15]
	v_pk_fma_f32 v[126:127], v[126:127], v[218:219], v[18:19]
	v_min_f32_e32 v122, 0x42700000, v122
	v_min_f32_e32 v123, 0x42700000, v123
	v_min_f32_e32 v126, 0x42700000, v126
	v_min_f32_e32 v127, 0x42700000, v127
	v_pk_fma_f32 v[124:125], v[124:125], v[216:217], v[16:17]
	v_pk_fma_f32 v[128:129], v[128:129], v[218:219], v[20:21]
	v_min_f32_e32 v124, 0x42700000, v124
	v_min_f32_e32 v125, 0x42700000, v125
	v_min_f32_e32 v128, 0x42700000, v128
	v_min_f32_e32 v129, 0x42700000, v129
	v_exp_f32_e32 v122, v122
	v_exp_f32_e32 v123, v123
	v_exp_f32_e32 v126, v126
	v_exp_f32_e32 v127, v127
	v_exp_f32_e32 v124, v124
	v_exp_f32_e32 v125, v125
	v_exp_f32_e32 v128, v128
	v_exp_f32_e32 v129, v129
	v_pk_fma_f32 v[228:229], v[122:123], v[10:11], v[10:11] neg_lo:[0,0,1] neg_hi:[0,0,1]
	v_pk_add_f32 v[126:127], v[126:127], v[222:223]
	v_pk_fma_f32 v[122:123], v[122:123], v[126:127], v[126:127]
	v_pk_fma_f32 v[230:231], v[124:125], v[12:13], v[12:13] neg_lo:[0,0,1] neg_hi:[0,0,1]
	v_pk_add_f32 v[128:129], v[128:129], v[222:223]
	v_pk_fma_f32 v[124:125], v[124:125], v[128:129], v[128:129]
	v_rcp_f32_e32 v122, v122
	v_rcp_f32_e32 v123, v123
	v_rcp_f32_e32 v124, v124
	v_rcp_f32_e32 v125, v125
	v_pk_fma_f32 v[202:203], v[228:229], v[122:123], v[202:203]
	v_pk_fma_f32 v[202:203], v[230:231], v[124:125], v[202:203]
	v_pk_fma_f32 v[118:119], v[118:119], v[216:217], v[34:35]
	v_pk_fma_f32 v[114:115], v[114:115], v[218:219], v[38:39]
	v_min_f32_e32 v118, 0x42700000, v118
	v_min_f32_e32 v119, 0x42700000, v119
	v_min_f32_e32 v114, 0x42700000, v114
	v_min_f32_e32 v115, 0x42700000, v115
	v_pk_fma_f32 v[120:121], v[120:121], v[216:217], v[36:37]
	v_pk_fma_f32 v[116:117], v[116:117], v[218:219], v[40:41]
	v_min_f32_e32 v120, 0x42700000, v120
	v_min_f32_e32 v121, 0x42700000, v121
	v_min_f32_e32 v116, 0x42700000, v116
	v_min_f32_e32 v117, 0x42700000, v117
	v_exp_f32_e32 v118, v118
	v_exp_f32_e32 v119, v119
	v_exp_f32_e32 v114, v114
	v_exp_f32_e32 v115, v115
	v_exp_f32_e32 v120, v120
	v_exp_f32_e32 v121, v121
	v_exp_f32_e32 v116, v116
	v_exp_f32_e32 v117, v117
	v_pk_fma_f32 v[228:229], v[118:119], v[30:31], v[30:31] neg_lo:[0,0,1] neg_hi:[0,0,1]
	v_pk_add_f32 v[114:115], v[114:115], v[222:223]
	v_pk_fma_f32 v[118:119], v[118:119], v[114:115], v[114:115]
	v_pk_fma_f32 v[230:231], v[120:121], v[32:33], v[32:33] neg_lo:[0,0,1] neg_hi:[0,0,1]
	v_pk_add_f32 v[116:117], v[116:117], v[222:223]
	v_pk_fma_f32 v[120:121], v[120:121], v[116:117], v[116:117]
	v_rcp_f32_e32 v118, v118
	v_rcp_f32_e32 v119, v119
	v_rcp_f32_e32 v120, v120
	v_rcp_f32_e32 v121, v121
	v_pk_mul_f32 v[204:205], v[228:229], v[118:119]
	v_pk_fma_f32 v[204:205], v[230:231], v[120:121], v[204:205]
	v_pk_fma_f32 v[106:107], v[106:107], v[216:217], v[14:15]
	v_pk_fma_f32 v[110:111], v[110:111], v[218:219], v[18:19]
	v_min_f32_e32 v106, 0x42700000, v106
	v_min_f32_e32 v107, 0x42700000, v107
	v_min_f32_e32 v110, 0x42700000, v110
	v_min_f32_e32 v111, 0x42700000, v111
	v_pk_fma_f32 v[108:109], v[108:109], v[216:217], v[16:17]
	v_pk_fma_f32 v[112:113], v[112:113], v[218:219], v[20:21]
	v_min_f32_e32 v108, 0x42700000, v108
	v_min_f32_e32 v109, 0x42700000, v109
	v_min_f32_e32 v112, 0x42700000, v112
	v_min_f32_e32 v113, 0x42700000, v113
	v_exp_f32_e32 v106, v106
	v_exp_f32_e32 v107, v107
	v_exp_f32_e32 v110, v110
	v_exp_f32_e32 v111, v111
	v_exp_f32_e32 v108, v108
	v_exp_f32_e32 v109, v109
	v_exp_f32_e32 v112, v112
	v_exp_f32_e32 v113, v113
	v_pk_fma_f32 v[228:229], v[106:107], v[10:11], v[10:11] neg_lo:[0,0,1] neg_hi:[0,0,1]
	v_pk_add_f32 v[110:111], v[110:111], v[222:223]
	v_pk_fma_f32 v[106:107], v[106:107], v[110:111], v[110:111]
	v_pk_fma_f32 v[230:231], v[108:109], v[12:13], v[12:13] neg_lo:[0,0,1] neg_hi:[0,0,1]
	v_pk_add_f32 v[112:113], v[112:113], v[222:223]
	v_pk_fma_f32 v[108:109], v[108:109], v[112:113], v[112:113]
	v_rcp_f32_e32 v106, v106
	v_rcp_f32_e32 v107, v107
	v_rcp_f32_e32 v108, v108
	v_rcp_f32_e32 v109, v109
	v_pk_fma_f32 v[204:205], v[228:229], v[106:107], v[204:205]
	v_pk_fma_f32 v[204:205], v[230:231], v[108:109], v[204:205]
	v_pk_fma_f32 v[102:103], v[102:103], v[216:217], v[34:35]
	v_pk_fma_f32 v[98:99], v[98:99], v[218:219], v[38:39]
	v_min_f32_e32 v102, 0x42700000, v102
	v_min_f32_e32 v103, 0x42700000, v103
	v_min_f32_e32 v98, 0x42700000, v98
	v_min_f32_e32 v99, 0x42700000, v99
	v_pk_fma_f32 v[104:105], v[104:105], v[216:217], v[36:37]
	v_pk_fma_f32 v[100:101], v[100:101], v[218:219], v[40:41]
	v_min_f32_e32 v104, 0x42700000, v104
	v_min_f32_e32 v105, 0x42700000, v105
	v_min_f32_e32 v100, 0x42700000, v100
	v_min_f32_e32 v101, 0x42700000, v101
	v_exp_f32_e32 v102, v102
	v_exp_f32_e32 v103, v103
	v_exp_f32_e32 v98, v98
	v_exp_f32_e32 v99, v99
	v_exp_f32_e32 v104, v104
	v_exp_f32_e32 v105, v105
	v_exp_f32_e32 v100, v100
	v_exp_f32_e32 v101, v101
	v_pk_fma_f32 v[228:229], v[102:103], v[30:31], v[30:31] neg_lo:[0,0,1] neg_hi:[0,0,1]
	v_pk_add_f32 v[98:99], v[98:99], v[222:223]
	v_pk_fma_f32 v[102:103], v[102:103], v[98:99], v[98:99]
	v_pk_fma_f32 v[230:231], v[104:105], v[32:33], v[32:33] neg_lo:[0,0,1] neg_hi:[0,0,1]
	v_pk_add_f32 v[100:101], v[100:101], v[222:223]
	v_pk_fma_f32 v[104:105], v[104:105], v[100:101], v[100:101]
	v_rcp_f32_e32 v102, v102
	v_rcp_f32_e32 v103, v103
	v_rcp_f32_e32 v104, v104
	v_rcp_f32_e32 v105, v105
	v_pk_mul_f32 v[206:207], v[228:229], v[102:103]
	v_pk_fma_f32 v[206:207], v[230:231], v[104:105], v[206:207]
	v_pk_fma_f32 v[90:91], v[90:91], v[216:217], v[14:15]
	v_pk_fma_f32 v[94:95], v[94:95], v[218:219], v[18:19]
	v_min_f32_e32 v90, 0x42700000, v90
	v_min_f32_e32 v91, 0x42700000, v91
	v_min_f32_e32 v94, 0x42700000, v94
	v_min_f32_e32 v95, 0x42700000, v95
	v_pk_fma_f32 v[92:93], v[92:93], v[216:217], v[16:17]
	v_pk_fma_f32 v[96:97], v[96:97], v[218:219], v[20:21]
	v_min_f32_e32 v92, 0x42700000, v92
	v_min_f32_e32 v93, 0x42700000, v93
	v_min_f32_e32 v96, 0x42700000, v96
	v_min_f32_e32 v97, 0x42700000, v97
	v_exp_f32_e32 v90, v90
	v_exp_f32_e32 v91, v91
	v_exp_f32_e32 v94, v94
	v_exp_f32_e32 v95, v95
	v_exp_f32_e32 v92, v92
	v_exp_f32_e32 v93, v93
	v_exp_f32_e32 v96, v96
	v_exp_f32_e32 v97, v97
	v_pk_fma_f32 v[228:229], v[90:91], v[10:11], v[10:11] neg_lo:[0,0,1] neg_hi:[0,0,1]
	v_pk_add_f32 v[94:95], v[94:95], v[222:223]
	v_pk_fma_f32 v[90:91], v[90:91], v[94:95], v[94:95]
	v_pk_fma_f32 v[230:231], v[92:93], v[12:13], v[12:13] neg_lo:[0,0,1] neg_hi:[0,0,1]
	v_pk_add_f32 v[96:97], v[96:97], v[222:223]
	v_pk_fma_f32 v[92:93], v[92:93], v[96:97], v[96:97]
	v_rcp_f32_e32 v90, v90
	v_rcp_f32_e32 v91, v91
	v_rcp_f32_e32 v92, v92
	v_rcp_f32_e32 v93, v93
	v_pk_fma_f32 v[206:207], v[228:229], v[90:91], v[206:207]
	v_pk_fma_f32 v[206:207], v[230:231], v[92:93], v[206:207]
	v_pk_fma_f32 v[86:87], v[86:87], v[216:217], v[34:35]
	v_pk_fma_f32 v[82:83], v[82:83], v[218:219], v[38:39]
	v_min_f32_e32 v86, 0x42700000, v86
	v_min_f32_e32 v87, 0x42700000, v87
	v_min_f32_e32 v82, 0x42700000, v82
	v_min_f32_e32 v83, 0x42700000, v83
	v_pk_fma_f32 v[88:89], v[88:89], v[216:217], v[36:37]
	v_pk_fma_f32 v[84:85], v[84:85], v[218:219], v[40:41]
	v_min_f32_e32 v88, 0x42700000, v88
	v_min_f32_e32 v89, 0x42700000, v89
	v_min_f32_e32 v84, 0x42700000, v84
	v_min_f32_e32 v85, 0x42700000, v85
	v_exp_f32_e32 v86, v86
	v_exp_f32_e32 v87, v87
	v_exp_f32_e32 v82, v82
	v_exp_f32_e32 v83, v83
	v_exp_f32_e32 v88, v88
	v_exp_f32_e32 v89, v89
	v_exp_f32_e32 v84, v84
	v_exp_f32_e32 v85, v85
	v_pk_fma_f32 v[228:229], v[86:87], v[30:31], v[30:31] neg_lo:[0,0,1] neg_hi:[0,0,1]
	v_pk_add_f32 v[82:83], v[82:83], v[222:223]
	v_pk_fma_f32 v[86:87], v[86:87], v[82:83], v[82:83]
	v_pk_fma_f32 v[230:231], v[88:89], v[32:33], v[32:33] neg_lo:[0,0,1] neg_hi:[0,0,1]
	v_pk_add_f32 v[84:85], v[84:85], v[222:223]
	v_pk_fma_f32 v[88:89], v[88:89], v[84:85], v[84:85]
	v_rcp_f32_e32 v86, v86
	v_rcp_f32_e32 v87, v87
	v_rcp_f32_e32 v88, v88
	v_rcp_f32_e32 v89, v89
	v_pk_mul_f32 v[208:209], v[228:229], v[86:87]
	v_pk_fma_f32 v[208:209], v[230:231], v[88:89], v[208:209]
	v_pk_fma_f32 v[74:75], v[74:75], v[216:217], v[14:15]
	v_pk_fma_f32 v[78:79], v[78:79], v[218:219], v[18:19]
	v_min_f32_e32 v74, 0x42700000, v74
	v_min_f32_e32 v75, 0x42700000, v75
	v_min_f32_e32 v78, 0x42700000, v78
	v_min_f32_e32 v79, 0x42700000, v79
	v_pk_fma_f32 v[76:77], v[76:77], v[216:217], v[16:17]
	v_pk_fma_f32 v[80:81], v[80:81], v[218:219], v[20:21]
	v_min_f32_e32 v76, 0x42700000, v76
	v_min_f32_e32 v77, 0x42700000, v77
	v_min_f32_e32 v80, 0x42700000, v80
	v_min_f32_e32 v81, 0x42700000, v81
	v_exp_f32_e32 v74, v74
	v_exp_f32_e32 v75, v75
	v_exp_f32_e32 v78, v78
	v_exp_f32_e32 v79, v79
	v_exp_f32_e32 v76, v76
	v_exp_f32_e32 v77, v77
	v_exp_f32_e32 v80, v80
	v_exp_f32_e32 v81, v81
	v_pk_fma_f32 v[228:229], v[74:75], v[10:11], v[10:11] neg_lo:[0,0,1] neg_hi:[0,0,1]
	v_pk_add_f32 v[78:79], v[78:79], v[222:223]
	v_pk_fma_f32 v[74:75], v[74:75], v[78:79], v[78:79]
	v_pk_fma_f32 v[230:231], v[76:77], v[12:13], v[12:13] neg_lo:[0,0,1] neg_hi:[0,0,1]
	v_pk_add_f32 v[80:81], v[80:81], v[222:223]
	v_pk_fma_f32 v[76:77], v[76:77], v[80:81], v[80:81]
	v_rcp_f32_e32 v74, v74
	v_rcp_f32_e32 v75, v75
	v_rcp_f32_e32 v76, v76
	v_rcp_f32_e32 v77, v77
	v_pk_fma_f32 v[208:209], v[228:229], v[74:75], v[208:209]
	v_pk_fma_f32 v[208:209], v[230:231], v[76:77], v[208:209]
	v_pk_fma_f32 v[70:71], v[70:71], v[216:217], v[34:35]
	v_pk_fma_f32 v[66:67], v[66:67], v[218:219], v[38:39]
	v_min_f32_e32 v70, 0x42700000, v70
	v_min_f32_e32 v71, 0x42700000, v71
	v_min_f32_e32 v66, 0x42700000, v66
	v_min_f32_e32 v67, 0x42700000, v67
	v_pk_fma_f32 v[72:73], v[72:73], v[216:217], v[36:37]
	v_pk_fma_f32 v[68:69], v[68:69], v[218:219], v[40:41]
	v_min_f32_e32 v72, 0x42700000, v72
	v_min_f32_e32 v73, 0x42700000, v73
	v_min_f32_e32 v68, 0x42700000, v68
	v_min_f32_e32 v69, 0x42700000, v69
	v_exp_f32_e32 v70, v70
	v_exp_f32_e32 v71, v71
	v_exp_f32_e32 v66, v66
	v_exp_f32_e32 v67, v67
	v_exp_f32_e32 v72, v72
	v_exp_f32_e32 v73, v73
	v_exp_f32_e32 v68, v68
	v_exp_f32_e32 v69, v69
	v_pk_fma_f32 v[228:229], v[70:71], v[30:31], v[30:31] neg_lo:[0,0,1] neg_hi:[0,0,1]
	v_pk_add_f32 v[66:67], v[66:67], v[222:223]
	v_pk_fma_f32 v[70:71], v[70:71], v[66:67], v[66:67]
	v_pk_fma_f32 v[230:231], v[72:73], v[32:33], v[32:33] neg_lo:[0,0,1] neg_hi:[0,0,1]
	v_pk_add_f32 v[68:69], v[68:69], v[222:223]
	v_pk_fma_f32 v[72:73], v[72:73], v[68:69], v[68:69]
	v_rcp_f32_e32 v70, v70
	v_rcp_f32_e32 v71, v71
	v_rcp_f32_e32 v72, v72
	v_rcp_f32_e32 v73, v73
	v_pk_mul_f32 v[210:211], v[228:229], v[70:71]
	v_pk_fma_f32 v[210:211], v[230:231], v[72:73], v[210:211]
	v_pk_fma_f32 v[58:59], v[58:59], v[216:217], v[14:15]
	v_pk_fma_f32 v[62:63], v[62:63], v[218:219], v[18:19]
	v_min_f32_e32 v58, 0x42700000, v58
	v_min_f32_e32 v59, 0x42700000, v59
	v_min_f32_e32 v62, 0x42700000, v62
	v_min_f32_e32 v63, 0x42700000, v63
	v_pk_fma_f32 v[60:61], v[60:61], v[216:217], v[16:17]
	v_pk_fma_f32 v[64:65], v[64:65], v[218:219], v[20:21]
	v_min_f32_e32 v60, 0x42700000, v60
	v_min_f32_e32 v61, 0x42700000, v61
	v_min_f32_e32 v64, 0x42700000, v64
	v_min_f32_e32 v65, 0x42700000, v65
	v_exp_f32_e32 v58, v58
	v_exp_f32_e32 v59, v59
	v_exp_f32_e32 v62, v62
	v_exp_f32_e32 v63, v63
	v_exp_f32_e32 v60, v60
	v_exp_f32_e32 v61, v61
	v_exp_f32_e32 v64, v64
	v_exp_f32_e32 v65, v65
	v_pk_fma_f32 v[228:229], v[58:59], v[10:11], v[10:11] neg_lo:[0,0,1] neg_hi:[0,0,1]
	v_pk_add_f32 v[62:63], v[62:63], v[222:223]
	v_pk_fma_f32 v[58:59], v[58:59], v[62:63], v[62:63]
	v_pk_fma_f32 v[230:231], v[60:61], v[12:13], v[12:13] neg_lo:[0,0,1] neg_hi:[0,0,1]
	v_pk_add_f32 v[64:65], v[64:65], v[222:223]
	v_pk_fma_f32 v[60:61], v[60:61], v[64:65], v[64:65]
	v_rcp_f32_e32 v58, v58
	v_rcp_f32_e32 v59, v59
	v_rcp_f32_e32 v60, v60
	v_rcp_f32_e32 v61, v61
	v_pk_fma_f32 v[210:211], v[228:229], v[58:59], v[210:211]
	v_pk_fma_f32 v[210:211], v[230:231], v[60:61], v[210:211]
	v_pk_fma_f32 v[54:55], v[54:55], v[216:217], v[34:35]
	v_pk_fma_f32 v[50:51], v[50:51], v[218:219], v[38:39]
	v_min_f32_e32 v54, 0x42700000, v54
	v_min_f32_e32 v55, 0x42700000, v55
	v_min_f32_e32 v50, 0x42700000, v50
	v_min_f32_e32 v51, 0x42700000, v51
	v_pk_fma_f32 v[56:57], v[56:57], v[216:217], v[36:37]
	v_pk_fma_f32 v[52:53], v[52:53], v[218:219], v[40:41]
	v_min_f32_e32 v56, 0x42700000, v56
	v_min_f32_e32 v57, 0x42700000, v57
	v_min_f32_e32 v52, 0x42700000, v52
	v_min_f32_e32 v53, 0x42700000, v53
	v_exp_f32_e32 v54, v54
	v_exp_f32_e32 v55, v55
	v_exp_f32_e32 v50, v50
	v_exp_f32_e32 v51, v51
	v_exp_f32_e32 v56, v56
	v_exp_f32_e32 v57, v57
	v_exp_f32_e32 v52, v52
	v_exp_f32_e32 v53, v53
	v_pk_fma_f32 v[228:229], v[54:55], v[30:31], v[30:31] neg_lo:[0,0,1] neg_hi:[0,0,1]
	v_pk_add_f32 v[50:51], v[50:51], v[222:223]
	v_pk_fma_f32 v[54:55], v[54:55], v[50:51], v[50:51]
	v_pk_fma_f32 v[230:231], v[56:57], v[32:33], v[32:33] neg_lo:[0,0,1] neg_hi:[0,0,1]
	v_pk_add_f32 v[52:53], v[52:53], v[222:223]
	v_pk_fma_f32 v[56:57], v[56:57], v[52:53], v[52:53]
	v_rcp_f32_e32 v54, v54
	v_rcp_f32_e32 v55, v55
	v_rcp_f32_e32 v56, v56
	v_rcp_f32_e32 v57, v57
	v_pk_mul_f32 v[212:213], v[228:229], v[54:55]
	v_pk_fma_f32 v[212:213], v[230:231], v[56:57], v[212:213]
	v_pk_fma_f32 v[42:43], v[42:43], v[216:217], v[14:15]
	v_pk_fma_f32 v[46:47], v[46:47], v[218:219], v[18:19]
	v_min_f32_e32 v42, 0x42700000, v42
	v_min_f32_e32 v43, 0x42700000, v43
	v_min_f32_e32 v46, 0x42700000, v46
	v_min_f32_e32 v47, 0x42700000, v47
	v_pk_fma_f32 v[44:45], v[44:45], v[216:217], v[16:17]
	v_pk_fma_f32 v[48:49], v[48:49], v[218:219], v[20:21]
	v_min_f32_e32 v44, 0x42700000, v44
	v_min_f32_e32 v45, 0x42700000, v45
	v_min_f32_e32 v48, 0x42700000, v48
	v_min_f32_e32 v49, 0x42700000, v49
	v_exp_f32_e32 v42, v42
	v_exp_f32_e32 v43, v43
	v_exp_f32_e32 v46, v46
	v_exp_f32_e32 v47, v47
	v_exp_f32_e32 v44, v44
	v_exp_f32_e32 v45, v45
	v_exp_f32_e32 v48, v48
	v_exp_f32_e32 v49, v49
	v_pk_fma_f32 v[228:229], v[42:43], v[10:11], v[10:11] neg_lo:[0,0,1] neg_hi:[0,0,1]
	v_pk_add_f32 v[46:47], v[46:47], v[222:223]
	v_pk_fma_f32 v[42:43], v[42:43], v[46:47], v[46:47]
	v_pk_fma_f32 v[230:231], v[44:45], v[12:13], v[12:13] neg_lo:[0,0,1] neg_hi:[0,0,1]
	v_pk_add_f32 v[48:49], v[48:49], v[222:223]
	v_pk_fma_f32 v[44:45], v[44:45], v[48:49], v[48:49]
	v_rcp_f32_e32 v42, v42
	v_rcp_f32_e32 v43, v43
	v_rcp_f32_e32 v44, v44
	v_rcp_f32_e32 v45, v45
	v_pk_fma_f32 v[212:213], v[228:229], v[42:43], v[212:213]
	v_pk_fma_f32 v[212:213], v[230:231], v[44:45], v[212:213]
	v_pk_fma_f32 v[26:27], v[26:27], v[216:217], v[34:35]
	v_pk_fma_f32 v[22:23], v[22:23], v[218:219], v[38:39]
	v_min_f32_e32 v26, 0x42700000, v26
	v_min_f32_e32 v27, 0x42700000, v27
	v_min_f32_e32 v22, 0x42700000, v22
	v_min_f32_e32 v23, 0x42700000, v23
	v_pk_fma_f32 v[28:29], v[28:29], v[216:217], v[36:37]
	v_pk_fma_f32 v[24:25], v[24:25], v[218:219], v[40:41]
	v_min_f32_e32 v28, 0x42700000, v28
	v_min_f32_e32 v29, 0x42700000, v29
	v_min_f32_e32 v24, 0x42700000, v24
	v_min_f32_e32 v25, 0x42700000, v25
	v_exp_f32_e32 v26, v26
	v_exp_f32_e32 v27, v27
	v_exp_f32_e32 v22, v22
	v_exp_f32_e32 v23, v23
	v_exp_f32_e32 v28, v28
	v_exp_f32_e32 v29, v29
	v_exp_f32_e32 v24, v24
	v_exp_f32_e32 v25, v25
	v_pk_fma_f32 v[228:229], v[26:27], v[30:31], v[30:31] neg_lo:[0,0,1] neg_hi:[0,0,1]
	v_pk_add_f32 v[22:23], v[22:23], v[222:223]
	v_pk_fma_f32 v[26:27], v[26:27], v[22:23], v[22:23]
	v_pk_fma_f32 v[230:231], v[28:29], v[32:33], v[32:33] neg_lo:[0,0,1] neg_hi:[0,0,1]
	v_pk_add_f32 v[24:25], v[24:25], v[222:223]
	v_pk_fma_f32 v[28:29], v[28:29], v[24:25], v[24:25]
	v_rcp_f32_e32 v26, v26
	v_rcp_f32_e32 v27, v27
	v_rcp_f32_e32 v28, v28
	v_rcp_f32_e32 v29, v29
	v_pk_mul_f32 v[214:215], v[228:229], v[26:27]
	v_pk_fma_f32 v[214:215], v[230:231], v[28:29], v[214:215]
	v_pk_fma_f32 v[2:3], v[2:3], v[216:217], v[14:15]
	v_pk_fma_f32 v[6:7], v[6:7], v[218:219], v[18:19]
	v_min_f32_e32 v2, 0x42700000, v2
	v_min_f32_e32 v3, 0x42700000, v3
	v_min_f32_e32 v6, 0x42700000, v6
	v_min_f32_e32 v7, 0x42700000, v7
	v_pk_fma_f32 v[4:5], v[4:5], v[216:217], v[16:17]
	v_pk_fma_f32 v[8:9], v[8:9], v[218:219], v[20:21]
	v_min_f32_e32 v4, 0x42700000, v4
	v_min_f32_e32 v5, 0x42700000, v5
	v_min_f32_e32 v8, 0x42700000, v8
	v_min_f32_e32 v9, 0x42700000, v9
	v_exp_f32_e32 v2, v2
	v_exp_f32_e32 v3, v3
	v_exp_f32_e32 v6, v6
	v_exp_f32_e32 v7, v7
	v_exp_f32_e32 v4, v4
	v_exp_f32_e32 v5, v5
	v_exp_f32_e32 v8, v8
	v_exp_f32_e32 v9, v9
	v_pk_fma_f32 v[228:229], v[2:3], v[10:11], v[10:11] neg_lo:[0,0,1] neg_hi:[0,0,1]
	v_pk_add_f32 v[6:7], v[6:7], v[222:223]
	v_pk_fma_f32 v[2:3], v[2:3], v[6:7], v[6:7]
	v_pk_fma_f32 v[230:231], v[4:5], v[12:13], v[12:13] neg_lo:[0,0,1] neg_hi:[0,0,1]
	v_pk_add_f32 v[8:9], v[8:9], v[222:223]
	v_pk_fma_f32 v[4:5], v[4:5], v[8:9], v[8:9]
	v_rcp_f32_e32 v2, v2
	v_rcp_f32_e32 v3, v3
	v_rcp_f32_e32 v4, v4
	v_rcp_f32_e32 v5, v5
	v_pk_fma_f32 v[214:215], v[228:229], v[2:3], v[214:215]
	v_pk_fma_f32 v[214:215], v[230:231], v[4:5], v[214:215]
	v_add_f32_e32 v240, v200, v201
	v_add_f32_e32 v241, v202, v203
	v_add_f32_e32 v242, v204, v205
	v_add_f32_e32 v243, v206, v207
	v_add_f32_e32 v244, v208, v209
	v_add_f32_e32 v245, v210, v211
	v_add_f32_e32 v246, v212, v213
	v_add_f32_e32 v247, v214, v215
	ds_bpermute_b32 v200, v181, v240
	ds_bpermute_b32 v201, v181, v241
	ds_bpermute_b32 v202, v181, v242
	ds_bpermute_b32 v203, v181, v243
	ds_bpermute_b32 v204, v181, v244
	ds_bpermute_b32 v205, v181, v245
	ds_bpermute_b32 v206, v181, v246
	ds_bpermute_b32 v207, v181, v247
	s_waitcnt lgkmcnt(0)
	v_add_f32_e32 v240, v240, v200
	v_add_f32_e32 v241, v241, v201
	v_add_f32_e32 v242, v242, v202
	v_add_f32_e32 v243, v243, v203
	v_add_f32_e32 v244, v244, v204
	v_add_f32_e32 v245, v245, v205
	v_add_f32_e32 v246, v246, v206
	v_add_f32_e32 v247, v247, v207
	ds_bpermute_b32 v200, v183, v240
	ds_bpermute_b32 v201, v183, v241
	ds_bpermute_b32 v202, v183, v242
	ds_bpermute_b32 v203, v183, v243
	ds_bpermute_b32 v204, v183, v244
	ds_bpermute_b32 v205, v183, v245
	ds_bpermute_b32 v206, v183, v246
	ds_bpermute_b32 v207, v183, v247
	s_waitcnt lgkmcnt(0)
	v_add_f32_e32 v240, v240, v200
	v_add_f32_e32 v241, v241, v201
	v_add_f32_e32 v242, v242, v202
	v_add_f32_e32 v243, v243, v203
	v_add_f32_e32 v244, v244, v204
	v_add_f32_e32 v245, v245, v205
	v_add_f32_e32 v246, v246, v206
	v_add_f32_e32 v247, v247, v207
	s_and_saveexec_b64 s[64:65], vcc
	ds_write2_b32 v232, v240, v241 offset0:0 offset1:16
	ds_write2_b32 v232, v242, v243 offset0:32 offset1:48
	ds_write2_b32 v232, v244, v245 offset0:64 offset1:80
	ds_write2_b32 v232, v246, v247 offset0:96 offset1:112
	s_mov_b64 exec, s[64:65]
	v_mov_b32_e32 v4, 0
	v_lshlrev_b32_e32 v10, 2, v189
	v_mov_b32_e32 v11, v4
	v_and_b32_e32 v70, 0x1c0, v0
	s_waitcnt lgkmcnt(0)
	v_lshl_add_u64 v[2:3], s[44:45], 0, v[10:11]
	s_lshl_b64 s[0:1], s[42:43], 17
	v_lshlrev_b32_e32 v6, 8, v70
	v_mov_b32_e32 v7, v4
	v_lshl_add_u64 v[2:3], v[2:3], 0, s[0:1]
	v_lshl_add_u64 v[2:3], v[2:3], 0, v[6:7]
	s_movk_i32 s0, 0x1000
	v_add_co_u32_e32 v6, vcc, s0, v2
	s_movk_i32 s0, 0x2000
	s_nop 0
	v_addc_co_u32_e32 v7, vcc, 0, v3, vcc
	v_add_co_u32_e32 v8, vcc, s0, v2
	s_movk_i32 s0, 0x3000
	s_nop 0
	v_addc_co_u32_e32 v9, vcc, 0, v3, vcc
	global_load_dword v78, v[2:3], off
	global_load_dword v77, v[2:3], off offset:256
	global_load_dword v76, v[2:3], off offset:512
	global_load_dword v75, v[2:3], off offset:768
	global_load_dword v74, v[2:3], off offset:1024
	global_load_dword v73, v[2:3], off offset:1280
	global_load_dword v72, v[2:3], off offset:1536
	global_load_dword v71, v[2:3], off offset:1792
	global_load_dword v69, v[2:3], off offset:2048
	global_load_dword v65, v[2:3], off offset:2304
	global_load_dword v63, v[2:3], off offset:2560
	global_load_dword v62, v[2:3], off offset:2816
	global_load_dword v61, v[2:3], off offset:3072
	global_load_dword v51, v[2:3], off offset:3328
	global_load_dword v52, v[2:3], off offset:3584
	global_load_dword v53, v[2:3], off offset:3840
	v_add_co_u32_e32 v2, vcc, s0, v2
	global_load_dword v55, v[6:7], off offset:256
	global_load_dword v56, v[6:7], off offset:512
	global_load_dword v57, v[6:7], off offset:768
	global_load_dword v54, v[6:7], off offset:1024
	global_load_dword v48, v[6:7], off offset:1280
	global_load_dword v49, v[6:7], off offset:1536
	global_load_dword v50, v[6:7], off offset:1792
	global_load_dword v47, v[6:7], off offset:2048
	global_load_dword v43, v[8:9], off
	global_load_dword v44, v[8:9], off offset:256
	global_load_dword v45, v[8:9], off offset:512
	global_load_dword v46, v[8:9], off offset:768
	global_load_dword v42, v[8:9], off offset:1024
	global_load_dword v39, v[8:9], off offset:1280
	global_load_dword v40, v[8:9], off offset:1536
	global_load_dword v41, v[8:9], off offset:1792
	global_load_dword v33, v[8:9], off offset:2048
	global_load_dword v34, v[8:9], off offset:2304
	global_load_dword v35, v[8:9], off offset:2560
	global_load_dword v36, v[8:9], off offset:2816
	global_load_dword v32, v[8:9], off offset:3072
	global_load_dword v24, v[8:9], off offset:3328
	global_load_dword v25, v[8:9], off offset:3584
	global_load_dword v26, v[8:9], off offset:3840
	v_addc_co_u32_e32 v3, vcc, 0, v3, vcc
	global_load_dword v66, v[6:7], off offset:2304
	global_load_dword v67, v[6:7], off offset:2560
	global_load_dword v68, v[6:7], off offset:2816
	global_load_dword v64, v[6:7], off offset:3072
	global_load_dword v58, v[6:7], off offset:3328
	global_load_dword v59, v[6:7], off offset:3584
	global_load_dword v60, v[6:7], off offset:3840
	global_load_dword v28, v[2:3], off
	global_load_dword v29, v[2:3], off offset:256
	global_load_dword v30, v[2:3], off offset:512
	global_load_dword v31, v[2:3], off offset:768
	global_load_dword v27, v[2:3], off offset:1024
	global_load_dword v21, v[2:3], off offset:1280
	global_load_dword v22, v[2:3], off offset:1536
	global_load_dword v23, v[2:3], off offset:1792
	global_load_dword v16, v[2:3], off offset:2048
	global_load_dword v79, v[8:9], off offset:-4096
	global_load_dword v18, v[2:3], off offset:2304
	global_load_dword v19, v[2:3], off offset:2560
	global_load_dword v20, v[2:3], off offset:2816
	global_load_dword v17, v[2:3], off offset:3072
	global_load_dword v15, v[2:3], off offset:3328
	global_load_dword v13, v[2:3], off offset:3584
	global_load_dword v11, v[2:3], off offset:3840
	v_lshl_add_u32 v2, v189, 2, 0
	v_add_u32_e32 v5, 0x20000, v2
	s_waitcnt vmcnt(63) expcnt(7) lgkmcnt(15)
	s_barrier
	ds_read2st64_b32 v[2:3], v5 offset1:1
	ds_read2st64_b32 v[6:7], v5 offset0:2 offset1:3
	ds_read2st64_b32 v[8:9], v5 offset0:4 offset1:5
	ds_read2st64_b32 v[80:81], v5 offset0:6 offset1:7
	s_mov_b32 s7, 0
	s_waitcnt lgkmcnt(3)
	v_add_f32_e32 v2, s2, v2
	v_add_f32_e32 v3, s2, v3
	s_waitcnt lgkmcnt(2)
	v_add_f32_e32 v2, v2, v6
	v_add_f32_e32 v3, v3, v7
	s_waitcnt lgkmcnt(1)
	v_add_f32_e32 v2, v2, v8
	v_add_f32_e32 v6, v3, v9
	s_waitcnt lgkmcnt(0)
	v_add_f32_e32 v12, v2, v80
	ds_read2st64_b32 v[2:3], v5 offset0:8 offset1:9
	v_add_f32_e32 v14, v6, v81
	ds_read2st64_b32 v[6:7], v5 offset0:10 offset1:11
	ds_read2st64_b32 v[8:9], v5 offset0:12 offset1:13
	ds_read2st64_b32 v[80:81], v5 offset0:14 offset1:15
	v_cmp_gt_u32_e64 s[0:1], 64, v0
	s_waitcnt lgkmcnt(3)
	v_add_f32_e32 v2, v12, v2
	v_add_f32_e32 v3, v14, v3
	s_waitcnt lgkmcnt(2)
	v_add_f32_e32 v2, v2, v6
	v_add_f32_e32 v3, v3, v7
	s_waitcnt lgkmcnt(1)
	v_add_f32_e32 v2, v2, v8
	v_add_f32_e32 v3, v3, v9
	s_waitcnt lgkmcnt(0)
	v_add_f32_e32 v2, v2, v80
	v_add_f32_e32 v3, v3, v81
	v_max_f32_e32 v5, v2, v3
	s_nop 1
	v_max_f32_dpp v5, v5, v5 quad_perm:[1,0,3,2] row_mask:0xf bank_mask:0xf
	s_nop 1
	v_max_f32_dpp v5, v5, v5 quad_perm:[2,3,0,1] row_mask:0xf bank_mask:0xf
	s_nop 1
	v_max_f32_dpp v5, v5, v5 row_half_mirror row_mask:0xf bank_mask:0xf
	s_nop 1
	v_max_f32_dpp v5, v5, v5 row_mirror row_mask:0xf bank_mask:0xf
	ds_bpermute_b32 v6, v181, v5
	s_waitcnt lgkmcnt(0)
	v_max_f32_e32 v5, v5, v6
	ds_bpermute_b32 v6, v183, v5
	s_waitcnt lgkmcnt(0)
	v_max_f32_e32 v14, v5, v6
	v_sub_f32_e32 v2, v2, v14
	v_sub_f32_e32 v3, v3, v14
	v_mul_f32_e32 v2, 0x3fb8aa3b, v2
	v_mul_f32_e32 v3, 0x3fb8aa3b, v3
	v_exp_f32_e32 v2, v2
	v_exp_f32_e32 v3, v3
	s_nop 0
	v_add_f32_e32 v5, v2, v3
	s_nop 1
	v_add_f32_dpp v5, v5, v5 quad_perm:[1,0,3,2] row_mask:0xf bank_mask:0xf
	s_nop 1
	v_add_f32_dpp v5, v5, v5 quad_perm:[2,3,0,1] row_mask:0xf bank_mask:0xf
	s_nop 1
	v_add_f32_dpp v5, v5, v5 row_half_mirror row_mask:0xf bank_mask:0xf
	s_nop 1
	v_add_f32_dpp v5, v5, v5 row_mirror row_mask:0xf bank_mask:0xf
	ds_bpermute_b32 v6, v181, v5
	s_waitcnt lgkmcnt(0)
	v_add_f32_e32 v37, v5, v6
	ds_bpermute_b32 v38, v183, v37
	s_and_saveexec_b64 s[2:3], s[0:1]
	s_cbranch_execz .LBB5_166
	s_add_i32 s12, 0, 0x21000
	v_lshl_add_u32 v5, v189, 2, s12
	v_lshl_add_u32 v6, v0, 2, s12
	ds_write_b32 v5, v2
	ds_write_b32 v6, v3 offset:256
